# speedup vs baseline: 1.0196x; 1.0196x over previous
.LBB0_3:
	s_load_dwordx4 s[4:7], s[0:1], 0x58
	s_load_dwordx4 s[8:11], s[0:1], 0x0
	s_cmpk_lt_u32 s2, 0x4c0
	s_cselect_b64 s[12:13], -1, 0
	s_movk_i32 s3, 0xff40
	s_and_b64 s[14:15], s[12:13], exec
	v_mov_b32_e32 v1, 0x42000000
	s_cselect_b32 s3, s3, 0xfffffb40
	v_cndmask_b32_e64 v34, v1, 1.0, s[12:13]
	s_waitcnt lgkmcnt(0)
	s_cselect_b32 s9, s9, s11
	s_cselect_b32 s8, s8, s10
	s_cselect_b32 s5, s5, s7
	s_cselect_b32 s4, s4, s6
	s_add_i32 s3, s2, s3
	s_lshl_b32 s6, s2, 2
	v_lshrrev_b32_e32 v1, 6, v0
	s_lshl_b32 s3, s3, 3
	v_and_or_b32 v1, s6, 28, v1
	v_lshlrev_b32_e32 v4, 3, v0
	s_and_b32 s3, s3, 0x7fffffc0
	v_bfe_u32 v35, v0, 2, 4
	v_lshlrev_b32_e32 v36, 7, v1
	v_mov_b32_e32 v37, 0
	v_and_b32_e32 v40, 24, v4
	v_or_b32_e32 v26, s3, v35
	v_lshl_add_u64 v[2:3], s[8:9], 0, v[36:37]
	v_lshlrev_b32_e32 v36, 2, v40
	v_mov_b32_e32 v27, v37
	v_lshl_add_u64 v[28:29], v[2:3], 0, v[36:37]
	v_lshlrev_b64 v[2:3], 12, v[26:27]
	v_lshl_add_u64 v[10:11], v[28:29], 0, v[2:3]
	v_or_b32_e32 v36, 16, v26
	global_load_dwordx4 v[2:5], v[10:11], off nt
	global_load_dwordx4 v[6:9], v[10:11], off offset:16 nt
	v_lshlrev_b64 v[10:11], 12, v[36:37]
	v_lshl_add_u64 v[18:19], v[28:29], 0, v[10:11]
	v_or_b32_e32 v36, 32, v26
	global_load_dwordx4 v[10:13], v[18:19], off nt
	global_load_dwordx4 v[14:17], v[18:19], off offset:16 nt
	v_lshlrev_b64 v[18:19], 12, v[36:37]
	v_or_b32_e32 v36, 48, v26
	v_lshl_add_u64 v[30:31], v[28:29], 0, v[18:19]
	v_lshlrev_b64 v[26:27], 12, v[36:37]
	global_load_dwordx4 v[18:21], v[30:31], off nt
	global_load_dwordx4 v[22:25], v[30:31], off offset:16 nt
	v_lshl_add_u64 v[38:39], v[28:29], 0, v[26:27]
	global_load_dwordx4 v[26:29], v[38:39], off nt
	global_load_dwordx4 v[30:33], v[38:39], off offset:16 nt
	v_mov_b32_e32 v39, v37
	v_lshlrev_b32_e32 v38, 1, v40
	v_lshl_add_u64 v[38:39], s[4:5], 0, v[38:39]
	s_and_b64 s[4:5], s[12:13], exec
	s_cselect_b32 s4, 13, 10
	v_lshlrev_b32_e32 v1, s4, v1
	v_add_u32_e32 v1, s3, v1
	v_or_b32_e32 v36, v1, v35
	v_lshlrev_b64 v[36:37], 6, v[36:37]
	v_lshl_add_u64 v[36:37], v[38:39], 0, v[36:37]
	s_waitcnt vmcnt(7)
	v_pk_mul_f32 v[4:5], v[34:35], v[4:5] op_sel_hi:[0,1]
	v_pk_mul_f32 v[2:3], v[34:35], v[2:3] op_sel_hi:[0,1]
	s_waitcnt vmcnt(6)
	v_pk_mul_f32 v[8:9], v[34:35], v[8:9] op_sel_hi:[0,1]
	v_pk_mul_f32 v[6:7], v[34:35], v[6:7] op_sel_hi:[0,1]
	v_cvt_pk_f16_f32 v2, v2, v3
	v_cvt_pk_f16_f32 v3, v4, v5
	v_cvt_pk_f16_f32 v4, v6, v7
	v_cvt_pk_f16_f32 v5, v8, v9
	s_waitcnt vmcnt(5)
	v_pk_mul_f32 v[6:7], v[34:35], v[12:13] op_sel_hi:[0,1]
	v_pk_mul_f32 v[8:9], v[34:35], v[10:11] op_sel_hi:[0,1]
	s_waitcnt vmcnt(4)
	v_pk_mul_f32 v[10:11], v[34:35], v[16:17] op_sel_hi:[0,1]
	v_pk_mul_f32 v[12:13], v[34:35], v[14:15] op_sel_hi:[0,1]
	global_store_dwordx4 v[36:37], v[2:5], off sc1
	s_nop 1
	v_cvt_pk_f16_f32 v2, v8, v9
	v_cvt_pk_f16_f32 v3, v6, v7
	v_cvt_pk_f16_f32 v4, v12, v13
	v_cvt_pk_f16_f32 v5, v10, v11
	s_waitcnt vmcnt(4)
	v_pk_mul_f32 v[6:7], v[34:35], v[20:21] op_sel_hi:[0,1]
	v_pk_mul_f32 v[8:9], v[34:35], v[18:19] op_sel_hi:[0,1]
	s_waitcnt vmcnt(3)
	v_pk_mul_f32 v[10:11], v[34:35], v[24:25] op_sel_hi:[0,1]
	v_pk_mul_f32 v[12:13], v[34:35], v[22:23] op_sel_hi:[0,1]
	global_store_dwordx4 v[36:37], v[2:5], off offset:1024 sc1
	s_nop 1
	v_cvt_pk_f16_f32 v2, v8, v9
	v_cvt_pk_f16_f32 v3, v6, v7
	v_cvt_pk_f16_f32 v4, v12, v13
	v_cvt_pk_f16_f32 v5, v10, v11
	s_waitcnt vmcnt(3)
	v_pk_mul_f32 v[6:7], v[34:35], v[28:29] op_sel_hi:[0,1]
	v_pk_mul_f32 v[8:9], v[34:35], v[26:27] op_sel_hi:[0,1]
	s_waitcnt vmcnt(2)
	v_pk_mul_f32 v[10:11], v[34:35], v[32:33] op_sel_hi:[0,1]
	v_pk_mul_f32 v[12:13], v[34:35], v[30:31] op_sel_hi:[0,1]
	global_store_dwordx4 v[36:37], v[2:5], off offset:2048 sc1
	s_nop 1
	v_cvt_pk_f16_f32 v2, v8, v9
	v_cvt_pk_f16_f32 v3, v6, v7
	v_cvt_pk_f16_f32 v4, v12, v13
	v_cvt_pk_f16_f32 v5, v10, v11
	global_store_dwordx4 v[36:37], v[2:5], off offset:3072 sc1
	s_cbranch_execnz .LBB0_2

.LBB0_8:
	s_or_b64 exec, exec, s[0:1]
	v_lshlrev_b32_e32 v0, 2, v128
	v_lshlrev_b32_e32 v102, 5, v1
	s_waitcnt lgkmcnt(0)
	s_barrier
	ds_write_b128 v100, v[66:69]
	ds_write_b128 v100, v[70:73] offset:4096
	ds_write_b128 v100, v[74:77] offset:8192
	ds_write_b128 v100, v[78:81] offset:12288
	ds_write_b128 v100, v[82:85] offset:16384
	ds_write_b128 v100, v[86:89] offset:20480
	ds_write_b128 v100, v[90:93] offset:24576
	s_waitcnt vmcnt(0)
	ds_write_b128 v100, v[94:97] offset:28672
	s_waitcnt lgkmcnt(0)
	s_barrier
	ds_read_b128 v[94:97], v0 offset:32768
	ds_read_b128 v[90:93], v0 offset:32832
	ds_read_b128 v[86:89], v0 offset:32896
	ds_read_b128 v[82:85], v0 offset:32960
	ds_read_b128 v[78:81], v0 offset:33024
	ds_read_b128 v[74:77], v0 offset:33088
	ds_read_b128 v[70:73], v0 offset:33152
	ds_read_b128 v[66:69], v0 offset:33216
	ds_read_b128 v[104:107], v102
	ds_read_b128 v[108:111], v102 offset:16
	s_ashr_i32 s0, s22, 6
	s_lshr_b32 s1, s3, 1
	s_mulk_i32 s1, 0xc00
	s_lshl_b32 s0, s0, 10
	s_waitcnt lgkmcnt(1)
	v_pk_fma_f32 v[62:63], v[94:95], v[104:105], v[62:63] op_sel_hi:[1,0,1]
	v_pk_fma_f32 v[64:65], v[96:97], v[104:105], v[64:65] op_sel_hi:[1,0,1]
	s_ashr_i32 s2, s1, 31
	s_ashr_i32 s3, s0, 31
	v_and_b32_e32 v0, 28, v98
	v_pk_fma_f32 v[64:65], v[92:93], v[104:105], v[64:65] op_sel:[0,1,0]
	v_pk_fma_f32 v[62:63], v[90:91], v[104:105], v[62:63] op_sel:[0,1,0]
	s_add_u32 s0, s1, s0
	v_lshlrev_b32_e32 v98, 1, v0
	v_pk_fma_f32 v[64:65], v[88:89], v[106:107], v[64:65] op_sel_hi:[1,0,1]
	v_pk_fma_f32 v[62:63], v[86:87], v[106:107], v[62:63] op_sel_hi:[1,0,1]
	v_mov_b32_e32 v0, v107
	s_addc_u32 s1, s2, s3
	v_pk_fma_f32 v[64:65], v[84:85], v[0:1], v[64:65] op_sel_hi:[1,0,1]
	v_pk_fma_f32 v[62:63], v[82:83], v[0:1], v[62:63] op_sel_hi:[1,0,1]
	s_lshl_b64 s[0:1], s[0:1], 6
	s_waitcnt lgkmcnt(0)
	v_pk_fma_f32 v[64:65], v[80:81], v[108:109], v[64:65] op_sel_hi:[1,0,1]
	v_pk_fma_f32 v[62:63], v[78:79], v[108:109], v[62:63] op_sel_hi:[1,0,1]
	s_add_u32 s0, s20, s0
	v_pk_fma_f32 v[64:65], v[76:77], v[108:109], v[64:65] op_sel:[0,1,0]
	v_pk_fma_f32 v[62:63], v[74:75], v[108:109], v[62:63] op_sel:[0,1,0]
	s_addc_u32 s1, s21, s1
	v_mov_b32_e32 v99, 0
	v_pk_fma_f32 v[64:65], v[72:73], v[110:111], v[64:65] op_sel_hi:[1,0,1]
	v_pk_fma_f32 v[62:63], v[70:71], v[110:111], v[62:63] op_sel_hi:[1,0,1]
	v_mov_b32_e32 v0, v111
	v_lshl_add_u64 v[100:101], s[0:1], 0, v[98:99]
	v_pk_fma_f32 v[64:65], v[68:69], v[0:1], v[64:65] op_sel_hi:[1,0,1]
	v_pk_fma_f32 v[62:63], v[66:67], v[0:1], v[62:63] op_sel_hi:[1,0,1]
	s_mov_b32 s0, 0x42000000
	v_pk_mul_f32 v[64:65], v[64:65], s[0:1] op_sel_hi:[1,0]
	v_pk_mul_f32 v[62:63], v[62:63], s[0:1] op_sel_hi:[1,0]
	v_cvt_pk_f16_f32 v105, v64, v65
	v_cvt_pk_f16_f32 v104, v62, v63
	ds_read_b128 v[62:65], v102 offset:2048
	v_lshlrev_b32_e32 v98, 6, v1
	v_lshl_add_u64 v[0:1], v[100:101], 0, v[98:99]
	global_store_dwordx2 v[0:1], v[104:105], off sc1
	ds_read_b128 v[104:107], v102 offset:2064
	s_waitcnt lgkmcnt(1)
	v_pk_fma_f32 v[58:59], v[94:95], v[62:63], v[58:59] op_sel_hi:[1,0,1]
	v_pk_fma_f32 v[60:61], v[96:97], v[62:63], v[60:61] op_sel_hi:[1,0,1]
	v_pk_fma_f32 v[58:59], v[90:91], v[62:63], v[58:59] op_sel:[0,1,0]
	v_pk_fma_f32 v[60:61], v[92:93], v[62:63], v[60:61] op_sel:[0,1,0]
	v_pk_fma_f32 v[58:59], v[86:87], v[64:65], v[58:59] op_sel_hi:[1,0,1]
	v_pk_fma_f32 v[60:61], v[88:89], v[64:65], v[60:61] op_sel_hi:[1,0,1]
	v_mov_b32_e32 v62, v65
	v_pk_fma_f32 v[60:61], v[84:85], v[62:63], v[60:61] op_sel_hi:[1,0,1]
	v_pk_fma_f32 v[58:59], v[82:83], v[62:63], v[58:59] op_sel_hi:[1,0,1]
	s_waitcnt lgkmcnt(0)
	v_pk_fma_f32 v[60:61], v[80:81], v[104:105], v[60:61] op_sel_hi:[1,0,1]
	v_pk_fma_f32 v[58:59], v[78:79], v[104:105], v[58:59] op_sel_hi:[1,0,1]
	v_pk_fma_f32 v[60:61], v[76:77], v[104:105], v[60:61] op_sel:[0,1,0]
	v_pk_fma_f32 v[58:59], v[74:75], v[104:105], v[58:59] op_sel:[0,1,0]
	v_pk_fma_f32 v[60:61], v[72:73], v[106:107], v[60:61] op_sel_hi:[1,0,1]
	v_pk_fma_f32 v[58:59], v[70:71], v[106:107], v[58:59] op_sel_hi:[1,0,1]
	v_mov_b32_e32 v62, v107
	v_pk_fma_f32 v[60:61], v[68:69], v[62:63], v[60:61] op_sel_hi:[1,0,1]
	v_pk_fma_f32 v[58:59], v[66:67], v[62:63], v[58:59] op_sel_hi:[1,0,1]
	v_pk_mul_f32 v[60:61], v[60:61], s[0:1] op_sel_hi:[1,0]
	v_pk_mul_f32 v[58:59], v[58:59], s[0:1] op_sel_hi:[1,0]
	v_cvt_pk_f16_f32 v63, v60, v61
	v_cvt_pk_f16_f32 v62, v58, v59
	ds_read_b128 v[58:61], v102 offset:4096
	s_movk_i32 s1, 0x2000
	v_add_co_u32_e32 v104, vcc, s1, v0
	s_nop 1
	v_addc_co_u32_e32 v105, vcc, 0, v1, vcc
	global_store_dwordx2 v[104:105], v[62:63], off offset:-4096 sc1
	ds_read_b128 v[62:65], v102 offset:4112
	s_waitcnt lgkmcnt(1)
	v_pk_fma_f32 v[54:55], v[94:95], v[58:59], v[54:55] op_sel_hi:[1,0,1]
	v_pk_fma_f32 v[56:57], v[96:97], v[58:59], v[56:57] op_sel_hi:[1,0,1]
	v_pk_fma_f32 v[54:55], v[90:91], v[58:59], v[54:55] op_sel:[0,1,0]
	v_pk_fma_f32 v[56:57], v[92:93], v[58:59], v[56:57] op_sel:[0,1,0]
	v_pk_fma_f32 v[54:55], v[86:87], v[60:61], v[54:55] op_sel_hi:[1,0,1]
	v_pk_fma_f32 v[56:57], v[88:89], v[60:61], v[56:57] op_sel_hi:[1,0,1]
	v_mov_b32_e32 v58, v61
	v_pk_fma_f32 v[56:57], v[84:85], v[58:59], v[56:57] op_sel_hi:[1,0,1]
	v_pk_fma_f32 v[54:55], v[82:83], v[58:59], v[54:55] op_sel_hi:[1,0,1]
	s_waitcnt lgkmcnt(0)
	v_pk_fma_f32 v[56:57], v[80:81], v[62:63], v[56:57] op_sel_hi:[1,0,1]
	v_pk_fma_f32 v[54:55], v[78:79], v[62:63], v[54:55] op_sel_hi:[1,0,1]
	v_pk_fma_f32 v[56:57], v[76:77], v[62:63], v[56:57] op_sel:[0,1,0]
	v_pk_fma_f32 v[54:55], v[74:75], v[62:63], v[54:55] op_sel:[0,1,0]
	v_pk_fma_f32 v[56:57], v[72:73], v[64:65], v[56:57] op_sel_hi:[1,0,1]
	v_pk_fma_f32 v[54:55], v[70:71], v[64:65], v[54:55] op_sel_hi:[1,0,1]
	v_mov_b32_e32 v58, v65
	v_pk_fma_f32 v[56:57], v[68:69], v[58:59], v[56:57] op_sel_hi:[1,0,1]
	v_pk_fma_f32 v[54:55], v[66:67], v[58:59], v[54:55] op_sel_hi:[1,0,1]
	v_pk_mul_f32 v[58:59], v[56:57], s[0:1] op_sel_hi:[1,0]
	v_pk_mul_f32 v[60:61], v[54:55], s[0:1] op_sel_hi:[1,0]
	ds_read_b128 v[54:57], v102 offset:6144
	v_cvt_pk_f16_f32 v60, v60, v61
	v_cvt_pk_f16_f32 v61, v58, v59
	global_store_dwordx2 v[104:105], v[60:61], off sc1
	ds_read_b128 v[58:61], v102 offset:6160
	s_waitcnt lgkmcnt(1)
	v_pk_fma_f32 v[50:51], v[94:95], v[54:55], v[50:51] op_sel_hi:[1,0,1]
	v_pk_fma_f32 v[52:53], v[96:97], v[54:55], v[52:53] op_sel_hi:[1,0,1]
	v_pk_fma_f32 v[50:51], v[90:91], v[54:55], v[50:51] op_sel:[0,1,0]
	v_pk_fma_f32 v[52:53], v[92:93], v[54:55], v[52:53] op_sel:[0,1,0]
	v_pk_fma_f32 v[50:51], v[86:87], v[56:57], v[50:51] op_sel_hi:[1,0,1]
	v_pk_fma_f32 v[52:53], v[88:89], v[56:57], v[52:53] op_sel_hi:[1,0,1]
	v_mov_b32_e32 v54, v57
	v_pk_fma_f32 v[52:53], v[84:85], v[54:55], v[52:53] op_sel_hi:[1,0,1]
	v_pk_fma_f32 v[50:51], v[82:83], v[54:55], v[50:51] op_sel_hi:[1,0,1]
	s_waitcnt lgkmcnt(0)
	v_pk_fma_f32 v[52:53], v[80:81], v[58:59], v[52:53] op_sel_hi:[1,0,1]
	v_pk_fma_f32 v[50:51], v[78:79], v[58:59], v[50:51] op_sel_hi:[1,0,1]
	v_pk_fma_f32 v[52:53], v[76:77], v[58:59], v[52:53] op_sel:[0,1,0]
	v_pk_fma_f32 v[50:51], v[74:75], v[58:59], v[50:51] op_sel:[0,1,0]
	v_pk_fma_f32 v[52:53], v[72:73], v[60:61], v[52:53] op_sel_hi:[1,0,1]
	v_pk_fma_f32 v[50:51], v[70:71], v[60:61], v[50:51] op_sel_hi:[1,0,1]
	v_mov_b32_e32 v54, v61
	v_pk_fma_f32 v[52:53], v[68:69], v[54:55], v[52:53] op_sel_hi:[1,0,1]
	v_pk_fma_f32 v[50:51], v[66:67], v[54:55], v[50:51] op_sel_hi:[1,0,1]
	v_pk_mul_f32 v[52:53], v[52:53], s[0:1] op_sel_hi:[1,0]
	v_pk_mul_f32 v[50:51], v[50:51], s[0:1] op_sel_hi:[1,0]
	v_cvt_pk_f16_f32 v55, v52, v53
	v_cvt_pk_f16_f32 v54, v50, v51
	ds_read_b128 v[50:53], v102 offset:8192
	s_movk_i32 s1, 0x3000
	v_add_co_u32_e32 v56, vcc, s1, v0
	s_nop 1
	v_addc_co_u32_e32 v57, vcc, 0, v1, vcc
	global_store_dwordx2 v[56:57], v[54:55], off sc1
	ds_read_b128 v[54:57], v102 offset:8208
	s_waitcnt lgkmcnt(1)
	v_pk_fma_f32 v[46:47], v[94:95], v[50:51], v[46:47] op_sel_hi:[1,0,1]
	v_pk_fma_f32 v[48:49], v[96:97], v[50:51], v[48:49] op_sel_hi:[1,0,1]
	v_pk_fma_f32 v[46:47], v[90:91], v[50:51], v[46:47] op_sel:[0,1,0]
	v_pk_fma_f32 v[48:49], v[92:93], v[50:51], v[48:49] op_sel:[0,1,0]
	v_pk_fma_f32 v[46:47], v[86:87], v[52:53], v[46:47] op_sel_hi:[1,0,1]
	v_pk_fma_f32 v[48:49], v[88:89], v[52:53], v[48:49] op_sel_hi:[1,0,1]
	v_mov_b32_e32 v50, v53
	v_pk_fma_f32 v[48:49], v[84:85], v[50:51], v[48:49] op_sel_hi:[1,0,1]
	v_pk_fma_f32 v[46:47], v[82:83], v[50:51], v[46:47] op_sel_hi:[1,0,1]
	s_waitcnt lgkmcnt(0)
	v_pk_fma_f32 v[48:49], v[80:81], v[54:55], v[48:49] op_sel_hi:[1,0,1]
	v_pk_fma_f32 v[46:47], v[78:79], v[54:55], v[46:47] op_sel_hi:[1,0,1]
	v_pk_fma_f32 v[48:49], v[76:77], v[54:55], v[48:49] op_sel:[0,1,0]
	v_pk_fma_f32 v[46:47], v[74:75], v[54:55], v[46:47] op_sel:[0,1,0]
	v_pk_fma_f32 v[48:49], v[72:73], v[56:57], v[48:49] op_sel_hi:[1,0,1]
	v_pk_fma_f32 v[46:47], v[70:71], v[56:57], v[46:47] op_sel_hi:[1,0,1]
	v_mov_b32_e32 v50, v57
	v_pk_fma_f32 v[48:49], v[68:69], v[50:51], v[48:49] op_sel_hi:[1,0,1]
	v_pk_fma_f32 v[46:47], v[66:67], v[50:51], v[46:47] op_sel_hi:[1,0,1]
	v_pk_mul_f32 v[48:49], v[48:49], s[0:1] op_sel_hi:[1,0]
	v_pk_mul_f32 v[46:47], v[46:47], s[0:1] op_sel_hi:[1,0]
	v_cvt_pk_f16_f32 v51, v48, v49
	v_cvt_pk_f16_f32 v50, v46, v47
	ds_read_b128 v[46:49], v102 offset:10240
	v_or_b32_e32 v52, 0x4000, v98
	v_mov_b32_e32 v53, v99
	v_lshl_add_u64 v[52:53], v[100:101], 0, v[52:53]
	global_store_dwordx2 v[52:53], v[50:51], off sc1
	ds_read_b128 v[50:53], v102 offset:10256
	s_waitcnt lgkmcnt(1)
	v_pk_fma_f32 v[42:43], v[94:95], v[46:47], v[42:43] op_sel_hi:[1,0,1]
	v_pk_fma_f32 v[44:45], v[96:97], v[46:47], v[44:45] op_sel_hi:[1,0,1]
	v_pk_fma_f32 v[42:43], v[90:91], v[46:47], v[42:43] op_sel:[0,1,0]
	v_pk_fma_f32 v[44:45], v[92:93], v[46:47], v[44:45] op_sel:[0,1,0]
	v_pk_fma_f32 v[42:43], v[86:87], v[48:49], v[42:43] op_sel_hi:[1,0,1]
	v_pk_fma_f32 v[44:45], v[88:89], v[48:49], v[44:45] op_sel_hi:[1,0,1]
	v_mov_b32_e32 v46, v49
	v_pk_fma_f32 v[44:45], v[84:85], v[46:47], v[44:45] op_sel_hi:[1,0,1]
	v_pk_fma_f32 v[42:43], v[82:83], v[46:47], v[42:43] op_sel_hi:[1,0,1]
	s_waitcnt lgkmcnt(0)
	v_pk_fma_f32 v[44:45], v[80:81], v[50:51], v[44:45] op_sel_hi:[1,0,1]
	v_pk_fma_f32 v[42:43], v[78:79], v[50:51], v[42:43] op_sel_hi:[1,0,1]
	v_pk_fma_f32 v[44:45], v[76:77], v[50:51], v[44:45] op_sel:[0,1,0]
	v_pk_fma_f32 v[42:43], v[74:75], v[50:51], v[42:43] op_sel:[0,1,0]
	v_pk_fma_f32 v[44:45], v[72:73], v[52:53], v[44:45] op_sel_hi:[1,0,1]
	v_pk_fma_f32 v[42:43], v[70:71], v[52:53], v[42:43] op_sel_hi:[1,0,1]
	v_mov_b32_e32 v46, v53
	v_pk_fma_f32 v[44:45], v[68:69], v[46:47], v[44:45] op_sel_hi:[1,0,1]
	v_pk_fma_f32 v[42:43], v[66:67], v[46:47], v[42:43] op_sel_hi:[1,0,1]
	v_pk_mul_f32 v[44:45], v[44:45], s[0:1] op_sel_hi:[1,0]
	v_pk_mul_f32 v[42:43], v[42:43], s[0:1] op_sel_hi:[1,0]
	v_cvt_pk_f16_f32 v47, v44, v45
	v_cvt_pk_f16_f32 v46, v42, v43
	ds_read_b128 v[42:45], v102 offset:12288
	s_movk_i32 s1, 0x6000
	v_add_co_u32_e32 v50, vcc, s1, v0
	s_nop 1
	v_addc_co_u32_e32 v51, vcc, 0, v1, vcc
	global_store_dwordx2 v[50:51], v[46:47], off offset:-4096 sc1
	ds_read_b128 v[46:49], v102 offset:12304
	s_waitcnt lgkmcnt(1)
	v_pk_fma_f32 v[38:39], v[94:95], v[42:43], v[38:39] op_sel_hi:[1,0,1]
	v_pk_fma_f32 v[40:41], v[96:97], v[42:43], v[40:41] op_sel_hi:[1,0,1]
	v_pk_fma_f32 v[38:39], v[90:91], v[42:43], v[38:39] op_sel:[0,1,0]
	v_pk_fma_f32 v[40:41], v[92:93], v[42:43], v[40:41] op_sel:[0,1,0]
	v_pk_fma_f32 v[38:39], v[86:87], v[44:45], v[38:39] op_sel_hi:[1,0,1]
	v_pk_fma_f32 v[40:41], v[88:89], v[44:45], v[40:41] op_sel_hi:[1,0,1]
	v_mov_b32_e32 v42, v45
	v_pk_fma_f32 v[40:41], v[84:85], v[42:43], v[40:41] op_sel_hi:[1,0,1]
	v_pk_fma_f32 v[38:39], v[82:83], v[42:43], v[38:39] op_sel_hi:[1,0,1]
	s_waitcnt lgkmcnt(0)
	v_pk_fma_f32 v[40:41], v[80:81], v[46:47], v[40:41] op_sel_hi:[1,0,1]
	v_pk_fma_f32 v[38:39], v[78:79], v[46:47], v[38:39] op_sel_hi:[1,0,1]
	v_pk_fma_f32 v[40:41], v[76:77], v[46:47], v[40:41] op_sel:[0,1,0]
	v_pk_fma_f32 v[38:39], v[74:75], v[46:47], v[38:39] op_sel:[0,1,0]
	v_pk_fma_f32 v[40:41], v[72:73], v[48:49], v[40:41] op_sel_hi:[1,0,1]
	v_pk_fma_f32 v[38:39], v[70:71], v[48:49], v[38:39] op_sel_hi:[1,0,1]
	v_mov_b32_e32 v42, v49
	v_pk_fma_f32 v[40:41], v[68:69], v[42:43], v[40:41] op_sel_hi:[1,0,1]
	v_pk_fma_f32 v[38:39], v[66:67], v[42:43], v[38:39] op_sel_hi:[1,0,1]
	v_pk_mul_f32 v[42:43], v[40:41], s[0:1] op_sel_hi:[1,0]
	v_pk_mul_f32 v[44:45], v[38:39], s[0:1] op_sel_hi:[1,0]
	ds_read_b128 v[38:41], v102 offset:14336
	v_cvt_pk_f16_f32 v44, v44, v45
	v_cvt_pk_f16_f32 v45, v42, v43
	global_store_dwordx2 v[50:51], v[44:45], off sc1
	ds_read_b128 v[42:45], v102 offset:14352
	s_waitcnt lgkmcnt(1)
	v_pk_fma_f32 v[34:35], v[94:95], v[38:39], v[34:35] op_sel_hi:[1,0,1]
	v_pk_fma_f32 v[36:37], v[96:97], v[38:39], v[36:37] op_sel_hi:[1,0,1]
	v_pk_fma_f32 v[34:35], v[90:91], v[38:39], v[34:35] op_sel:[0,1,0]
	v_pk_fma_f32 v[36:37], v[92:93], v[38:39], v[36:37] op_sel:[0,1,0]
	v_pk_fma_f32 v[34:35], v[86:87], v[40:41], v[34:35] op_sel_hi:[1,0,1]
	v_pk_fma_f32 v[36:37], v[88:89], v[40:41], v[36:37] op_sel_hi:[1,0,1]
	v_mov_b32_e32 v38, v41
	v_pk_fma_f32 v[36:37], v[84:85], v[38:39], v[36:37] op_sel_hi:[1,0,1]
	v_pk_fma_f32 v[34:35], v[82:83], v[38:39], v[34:35] op_sel_hi:[1,0,1]
	s_waitcnt lgkmcnt(0)
	v_pk_fma_f32 v[36:37], v[80:81], v[42:43], v[36:37] op_sel_hi:[1,0,1]
	v_pk_fma_f32 v[34:35], v[78:79], v[42:43], v[34:35] op_sel_hi:[1,0,1]
	v_pk_fma_f32 v[36:37], v[76:77], v[42:43], v[36:37] op_sel:[0,1,0]
	v_pk_fma_f32 v[34:35], v[74:75], v[42:43], v[34:35] op_sel:[0,1,0]
	v_pk_fma_f32 v[36:37], v[72:73], v[44:45], v[36:37] op_sel_hi:[1,0,1]
	v_pk_fma_f32 v[34:35], v[70:71], v[44:45], v[34:35] op_sel_hi:[1,0,1]
	v_mov_b32_e32 v38, v45
	v_pk_fma_f32 v[36:37], v[68:69], v[38:39], v[36:37] op_sel_hi:[1,0,1]
	v_pk_fma_f32 v[34:35], v[66:67], v[38:39], v[34:35] op_sel_hi:[1,0,1]
	v_pk_mul_f32 v[36:37], v[36:37], s[0:1] op_sel_hi:[1,0]
	v_pk_mul_f32 v[34:35], v[34:35], s[0:1] op_sel_hi:[1,0]
	v_cvt_pk_f16_f32 v39, v36, v37
	v_cvt_pk_f16_f32 v38, v34, v35
	ds_read_b128 v[34:37], v102 offset:16384
	s_movk_i32 s1, 0x7000
	v_add_co_u32_e32 v40, vcc, s1, v0
	s_nop 1
	v_addc_co_u32_e32 v41, vcc, 0, v1, vcc
	global_store_dwordx2 v[40:41], v[38:39], off sc1
	ds_read_b128 v[38:41], v102 offset:16400
	s_waitcnt lgkmcnt(1)
	v_pk_fma_f32 v[30:31], v[94:95], v[34:35], v[30:31] op_sel_hi:[1,0,1]
	v_pk_fma_f32 v[32:33], v[96:97], v[34:35], v[32:33] op_sel_hi:[1,0,1]
	v_pk_fma_f32 v[30:31], v[90:91], v[34:35], v[30:31] op_sel:[0,1,0]
	v_pk_fma_f32 v[32:33], v[92:93], v[34:35], v[32:33] op_sel:[0,1,0]
	v_pk_fma_f32 v[30:31], v[86:87], v[36:37], v[30:31] op_sel_hi:[1,0,1]
	v_pk_fma_f32 v[32:33], v[88:89], v[36:37], v[32:33] op_sel_hi:[1,0,1]
	v_mov_b32_e32 v34, v37
	v_pk_fma_f32 v[32:33], v[84:85], v[34:35], v[32:33] op_sel_hi:[1,0,1]
	v_pk_fma_f32 v[30:31], v[82:83], v[34:35], v[30:31] op_sel_hi:[1,0,1]
	s_waitcnt lgkmcnt(0)
	v_pk_fma_f32 v[32:33], v[80:81], v[38:39], v[32:33] op_sel_hi:[1,0,1]
	v_pk_fma_f32 v[30:31], v[78:79], v[38:39], v[30:31] op_sel_hi:[1,0,1]
	v_pk_fma_f32 v[32:33], v[76:77], v[38:39], v[32:33] op_sel:[0,1,0]
	v_pk_fma_f32 v[30:31], v[74:75], v[38:39], v[30:31] op_sel:[0,1,0]
	v_pk_fma_f32 v[32:33], v[72:73], v[40:41], v[32:33] op_sel_hi:[1,0,1]
	v_pk_fma_f32 v[30:31], v[70:71], v[40:41], v[30:31] op_sel_hi:[1,0,1]
	v_mov_b32_e32 v34, v41
	v_pk_fma_f32 v[32:33], v[68:69], v[34:35], v[32:33] op_sel_hi:[1,0,1]
	v_pk_fma_f32 v[30:31], v[66:67], v[34:35], v[30:31] op_sel_hi:[1,0,1]
	v_pk_mul_f32 v[32:33], v[32:33], s[0:1] op_sel_hi:[1,0]
	v_pk_mul_f32 v[30:31], v[30:31], s[0:1] op_sel_hi:[1,0]
	v_cvt_pk_f16_f32 v35, v32, v33
	v_cvt_pk_f16_f32 v34, v30, v31
	ds_read_b128 v[30:33], v102 offset:18432
	v_or_b32_e32 v36, 0x8000, v98
	v_mov_b32_e32 v37, v99
	v_lshl_add_u64 v[36:37], v[100:101], 0, v[36:37]
	global_store_dwordx2 v[36:37], v[34:35], off sc1
	ds_read_b128 v[34:37], v102 offset:18448
	s_waitcnt lgkmcnt(1)
	v_pk_fma_f32 v[26:27], v[94:95], v[30:31], v[26:27] op_sel_hi:[1,0,1]
	v_pk_fma_f32 v[28:29], v[96:97], v[30:31], v[28:29] op_sel_hi:[1,0,1]
	v_pk_fma_f32 v[26:27], v[90:91], v[30:31], v[26:27] op_sel:[0,1,0]
	v_pk_fma_f32 v[28:29], v[92:93], v[30:31], v[28:29] op_sel:[0,1,0]
	v_pk_fma_f32 v[26:27], v[86:87], v[32:33], v[26:27] op_sel_hi:[1,0,1]
	v_pk_fma_f32 v[28:29], v[88:89], v[32:33], v[28:29] op_sel_hi:[1,0,1]
	v_mov_b32_e32 v30, v33
	v_pk_fma_f32 v[28:29], v[84:85], v[30:31], v[28:29] op_sel_hi:[1,0,1]
	v_pk_fma_f32 v[26:27], v[82:83], v[30:31], v[26:27] op_sel_hi:[1,0,1]
	s_waitcnt lgkmcnt(0)
	v_pk_fma_f32 v[28:29], v[80:81], v[34:35], v[28:29] op_sel_hi:[1,0,1]
	v_pk_fma_f32 v[26:27], v[78:79], v[34:35], v[26:27] op_sel_hi:[1,0,1]
	v_pk_fma_f32 v[28:29], v[76:77], v[34:35], v[28:29] op_sel:[0,1,0]
	v_pk_fma_f32 v[26:27], v[74:75], v[34:35], v[26:27] op_sel:[0,1,0]
	v_pk_fma_f32 v[28:29], v[72:73], v[36:37], v[28:29] op_sel_hi:[1,0,1]
	v_pk_fma_f32 v[26:27], v[70:71], v[36:37], v[26:27] op_sel_hi:[1,0,1]
	v_mov_b32_e32 v30, v37
	v_pk_fma_f32 v[28:29], v[68:69], v[30:31], v[28:29] op_sel_hi:[1,0,1]
	v_pk_fma_f32 v[26:27], v[66:67], v[30:31], v[26:27] op_sel_hi:[1,0,1]
	v_pk_mul_f32 v[28:29], v[28:29], s[0:1] op_sel_hi:[1,0]
	v_pk_mul_f32 v[26:27], v[26:27], s[0:1] op_sel_hi:[1,0]
	v_cvt_pk_f16_f32 v31, v28, v29
	v_cvt_pk_f16_f32 v30, v26, v27
	ds_read_b128 v[26:29], v102 offset:20480
	s_mov_b32 s1, 0xa000
	v_add_co_u32_e32 v34, vcc, s1, v0
	v_or_b32_e32 v98, 0xc000, v98
	s_nop 0
	v_addc_co_u32_e32 v35, vcc, 0, v1, vcc
	global_store_dwordx2 v[34:35], v[30:31], off offset:-4096 sc1
	ds_read_b128 v[30:33], v102 offset:20496
	s_waitcnt lgkmcnt(1)
	v_pk_fma_f32 v[22:23], v[94:95], v[26:27], v[22:23] op_sel_hi:[1,0,1]
	v_pk_fma_f32 v[24:25], v[96:97], v[26:27], v[24:25] op_sel_hi:[1,0,1]
	v_pk_fma_f32 v[22:23], v[90:91], v[26:27], v[22:23] op_sel:[0,1,0]
	v_pk_fma_f32 v[24:25], v[92:93], v[26:27], v[24:25] op_sel:[0,1,0]
	v_pk_fma_f32 v[22:23], v[86:87], v[28:29], v[22:23] op_sel_hi:[1,0,1]
	v_pk_fma_f32 v[24:25], v[88:89], v[28:29], v[24:25] op_sel_hi:[1,0,1]
	v_mov_b32_e32 v26, v29
	v_pk_fma_f32 v[24:25], v[84:85], v[26:27], v[24:25] op_sel_hi:[1,0,1]
	v_pk_fma_f32 v[22:23], v[82:83], v[26:27], v[22:23] op_sel_hi:[1,0,1]
	s_waitcnt lgkmcnt(0)
	v_pk_fma_f32 v[24:25], v[80:81], v[30:31], v[24:25] op_sel_hi:[1,0,1]
	v_pk_fma_f32 v[22:23], v[78:79], v[30:31], v[22:23] op_sel_hi:[1,0,1]
	v_pk_fma_f32 v[24:25], v[76:77], v[30:31], v[24:25] op_sel:[0,1,0]
	v_pk_fma_f32 v[22:23], v[74:75], v[30:31], v[22:23] op_sel:[0,1,0]
	v_pk_fma_f32 v[24:25], v[72:73], v[32:33], v[24:25] op_sel_hi:[1,0,1]
	v_pk_fma_f32 v[22:23], v[70:71], v[32:33], v[22:23] op_sel_hi:[1,0,1]
	v_mov_b32_e32 v26, v33
	v_pk_fma_f32 v[24:25], v[68:69], v[26:27], v[24:25] op_sel_hi:[1,0,1]
	v_pk_fma_f32 v[22:23], v[66:67], v[26:27], v[22:23] op_sel_hi:[1,0,1]
	v_pk_mul_f32 v[26:27], v[24:25], s[0:1] op_sel_hi:[1,0]
	v_pk_mul_f32 v[28:29], v[22:23], s[0:1] op_sel_hi:[1,0]
	ds_read_b128 v[22:25], v102 offset:22528
	v_cvt_pk_f16_f32 v28, v28, v29
	v_cvt_pk_f16_f32 v29, v26, v27
	global_store_dwordx2 v[34:35], v[28:29], off sc1
	ds_read_b128 v[26:29], v102 offset:22544
	s_waitcnt lgkmcnt(1)
	v_pk_fma_f32 v[18:19], v[94:95], v[22:23], v[18:19] op_sel_hi:[1,0,1]
	v_pk_fma_f32 v[20:21], v[96:97], v[22:23], v[20:21] op_sel_hi:[1,0,1]
	v_pk_fma_f32 v[18:19], v[90:91], v[22:23], v[18:19] op_sel:[0,1,0]
	v_pk_fma_f32 v[20:21], v[92:93], v[22:23], v[20:21] op_sel:[0,1,0]
	v_pk_fma_f32 v[18:19], v[86:87], v[24:25], v[18:19] op_sel_hi:[1,0,1]
	v_pk_fma_f32 v[20:21], v[88:89], v[24:25], v[20:21] op_sel_hi:[1,0,1]
	v_mov_b32_e32 v22, v25
	v_pk_fma_f32 v[20:21], v[84:85], v[22:23], v[20:21] op_sel_hi:[1,0,1]
	v_pk_fma_f32 v[18:19], v[82:83], v[22:23], v[18:19] op_sel_hi:[1,0,1]
	s_waitcnt lgkmcnt(0)
	v_pk_fma_f32 v[20:21], v[80:81], v[26:27], v[20:21] op_sel_hi:[1,0,1]
	v_pk_fma_f32 v[18:19], v[78:79], v[26:27], v[18:19] op_sel_hi:[1,0,1]
	v_pk_fma_f32 v[20:21], v[76:77], v[26:27], v[20:21] op_sel:[0,1,0]
	v_pk_fma_f32 v[18:19], v[74:75], v[26:27], v[18:19] op_sel:[0,1,0]
	v_pk_fma_f32 v[20:21], v[72:73], v[28:29], v[20:21] op_sel_hi:[1,0,1]
	v_pk_fma_f32 v[18:19], v[70:71], v[28:29], v[18:19] op_sel_hi:[1,0,1]
	v_mov_b32_e32 v22, v29
	v_pk_fma_f32 v[20:21], v[68:69], v[22:23], v[20:21] op_sel_hi:[1,0,1]
	v_pk_fma_f32 v[18:19], v[66:67], v[22:23], v[18:19] op_sel_hi:[1,0,1]
	v_pk_mul_f32 v[20:21], v[20:21], s[0:1] op_sel_hi:[1,0]
	v_pk_mul_f32 v[18:19], v[18:19], s[0:1] op_sel_hi:[1,0]
	v_cvt_pk_f16_f32 v23, v20, v21
	v_cvt_pk_f16_f32 v22, v18, v19
	ds_read_b128 v[18:21], v102 offset:24576
	s_mov_b32 s1, 0xb000
	v_add_co_u32_e32 v24, vcc, s1, v0
	s_nop 1
	v_addc_co_u32_e32 v25, vcc, 0, v1, vcc
	global_store_dwordx2 v[24:25], v[22:23], off sc1
	ds_read_b128 v[22:25], v102 offset:24592
	s_waitcnt lgkmcnt(1)
	v_pk_fma_f32 v[14:15], v[94:95], v[18:19], v[14:15] op_sel_hi:[1,0,1]
	v_pk_fma_f32 v[16:17], v[96:97], v[18:19], v[16:17] op_sel_hi:[1,0,1]
	v_pk_fma_f32 v[14:15], v[90:91], v[18:19], v[14:15] op_sel:[0,1,0]
	v_pk_fma_f32 v[16:17], v[92:93], v[18:19], v[16:17] op_sel:[0,1,0]
	v_pk_fma_f32 v[14:15], v[86:87], v[20:21], v[14:15] op_sel_hi:[1,0,1]
	v_pk_fma_f32 v[16:17], v[88:89], v[20:21], v[16:17] op_sel_hi:[1,0,1]
	v_mov_b32_e32 v18, v21
	v_pk_fma_f32 v[16:17], v[84:85], v[18:19], v[16:17] op_sel_hi:[1,0,1]
	v_pk_fma_f32 v[14:15], v[82:83], v[18:19], v[14:15] op_sel_hi:[1,0,1]
	s_waitcnt lgkmcnt(0)
	v_pk_fma_f32 v[16:17], v[80:81], v[22:23], v[16:17] op_sel_hi:[1,0,1]
	v_pk_fma_f32 v[14:15], v[78:79], v[22:23], v[14:15] op_sel_hi:[1,0,1]
	v_pk_fma_f32 v[16:17], v[76:77], v[22:23], v[16:17] op_sel:[0,1,0]
	v_pk_fma_f32 v[14:15], v[74:75], v[22:23], v[14:15] op_sel:[0,1,0]
	v_pk_fma_f32 v[16:17], v[72:73], v[24:25], v[16:17] op_sel_hi:[1,0,1]
	v_pk_fma_f32 v[14:15], v[70:71], v[24:25], v[14:15] op_sel_hi:[1,0,1]
	v_mov_b32_e32 v18, v25
	v_pk_fma_f32 v[16:17], v[68:69], v[18:19], v[16:17] op_sel_hi:[1,0,1]
	v_pk_fma_f32 v[14:15], v[66:67], v[18:19], v[14:15] op_sel_hi:[1,0,1]
	v_pk_mul_f32 v[16:17], v[16:17], s[0:1] op_sel_hi:[1,0]
	v_pk_mul_f32 v[14:15], v[14:15], s[0:1] op_sel_hi:[1,0]
	v_cvt_pk_f16_f32 v19, v16, v17
	v_cvt_pk_f16_f32 v18, v14, v15
	ds_read_b128 v[14:17], v102 offset:26624
	v_lshl_add_u64 v[20:21], v[100:101], 0, v[98:99]
	global_store_dwordx2 v[20:21], v[18:19], off sc1
	ds_read_b128 v[18:21], v102 offset:26640
	s_waitcnt lgkmcnt(1)
	v_pk_fma_f32 v[10:11], v[94:95], v[14:15], v[10:11] op_sel_hi:[1,0,1]
	v_pk_fma_f32 v[12:13], v[96:97], v[14:15], v[12:13] op_sel_hi:[1,0,1]
	v_pk_fma_f32 v[10:11], v[90:91], v[14:15], v[10:11] op_sel:[0,1,0]
	v_pk_fma_f32 v[12:13], v[92:93], v[14:15], v[12:13] op_sel:[0,1,0]
	v_pk_fma_f32 v[10:11], v[86:87], v[16:17], v[10:11] op_sel_hi:[1,0,1]
	v_pk_fma_f32 v[12:13], v[88:89], v[16:17], v[12:13] op_sel_hi:[1,0,1]
	v_mov_b32_e32 v14, v17
	v_pk_fma_f32 v[12:13], v[84:85], v[14:15], v[12:13] op_sel_hi:[1,0,1]
	v_pk_fma_f32 v[10:11], v[82:83], v[14:15], v[10:11] op_sel_hi:[1,0,1]
	s_waitcnt lgkmcnt(0)
	v_pk_fma_f32 v[12:13], v[80:81], v[18:19], v[12:13] op_sel_hi:[1,0,1]
	v_pk_fma_f32 v[10:11], v[78:79], v[18:19], v[10:11] op_sel_hi:[1,0,1]
	v_pk_fma_f32 v[12:13], v[76:77], v[18:19], v[12:13] op_sel:[0,1,0]
	v_pk_fma_f32 v[10:11], v[74:75], v[18:19], v[10:11] op_sel:[0,1,0]
	v_pk_fma_f32 v[12:13], v[72:73], v[20:21], v[12:13] op_sel_hi:[1,0,1]
	v_pk_fma_f32 v[10:11], v[70:71], v[20:21], v[10:11] op_sel_hi:[1,0,1]
	v_mov_b32_e32 v14, v21
	v_pk_fma_f32 v[12:13], v[68:69], v[14:15], v[12:13] op_sel_hi:[1,0,1]
	v_pk_fma_f32 v[10:11], v[66:67], v[14:15], v[10:11] op_sel_hi:[1,0,1]
	v_pk_mul_f32 v[12:13], v[12:13], s[0:1] op_sel_hi:[1,0]
	v_pk_mul_f32 v[10:11], v[10:11], s[0:1] op_sel_hi:[1,0]
	v_cvt_pk_f16_f32 v15, v12, v13
	v_cvt_pk_f16_f32 v14, v10, v11
	ds_read_b128 v[10:13], v102 offset:28672
	s_mov_b32 s1, 0xe000
	v_add_co_u32_e32 v18, vcc, s1, v0
	s_nop 1
	v_addc_co_u32_e32 v19, vcc, 0, v1, vcc
	global_store_dwordx2 v[18:19], v[14:15], off offset:-4096 sc1
	ds_read_b128 v[14:17], v102 offset:28688
	s_waitcnt lgkmcnt(1)
	v_pk_fma_f32 v[6:7], v[94:95], v[10:11], v[6:7] op_sel_hi:[1,0,1]
	v_pk_fma_f32 v[8:9], v[96:97], v[10:11], v[8:9] op_sel_hi:[1,0,1]
	v_pk_fma_f32 v[6:7], v[90:91], v[10:11], v[6:7] op_sel:[0,1,0]
	v_pk_fma_f32 v[8:9], v[92:93], v[10:11], v[8:9] op_sel:[0,1,0]
	v_pk_fma_f32 v[6:7], v[86:87], v[12:13], v[6:7] op_sel_hi:[1,0,1]
	v_pk_fma_f32 v[8:9], v[88:89], v[12:13], v[8:9] op_sel_hi:[1,0,1]
	v_mov_b32_e32 v10, v13
	v_pk_fma_f32 v[8:9], v[84:85], v[10:11], v[8:9] op_sel_hi:[1,0,1]
	v_pk_fma_f32 v[6:7], v[82:83], v[10:11], v[6:7] op_sel_hi:[1,0,1]
	s_waitcnt lgkmcnt(0)
	v_pk_fma_f32 v[8:9], v[80:81], v[14:15], v[8:9] op_sel_hi:[1,0,1]
	v_pk_fma_f32 v[6:7], v[78:79], v[14:15], v[6:7] op_sel_hi:[1,0,1]
	v_pk_fma_f32 v[8:9], v[76:77], v[14:15], v[8:9] op_sel:[0,1,0]
	v_pk_fma_f32 v[6:7], v[74:75], v[14:15], v[6:7] op_sel:[0,1,0]
	v_pk_fma_f32 v[8:9], v[72:73], v[16:17], v[8:9] op_sel_hi:[1,0,1]
	v_pk_fma_f32 v[6:7], v[70:71], v[16:17], v[6:7] op_sel_hi:[1,0,1]
	v_mov_b32_e32 v10, v17
	v_pk_fma_f32 v[8:9], v[68:69], v[10:11], v[8:9] op_sel_hi:[1,0,1]
	v_pk_fma_f32 v[6:7], v[66:67], v[10:11], v[6:7] op_sel_hi:[1,0,1]
	v_pk_mul_f32 v[10:11], v[8:9], s[0:1] op_sel_hi:[1,0]
	v_pk_mul_f32 v[12:13], v[6:7], s[0:1] op_sel_hi:[1,0]
	ds_read_b128 v[6:9], v102 offset:30720
	v_cvt_pk_f16_f32 v12, v12, v13
	v_cvt_pk_f16_f32 v13, v10, v11
	global_store_dwordx2 v[18:19], v[12:13], off sc1
	ds_read_b128 v[10:13], v102 offset:30736
	s_waitcnt lgkmcnt(1)
	v_pk_fma_f32 v[2:3], v[94:95], v[6:7], v[2:3] op_sel_hi:[1,0,1]
	v_pk_fma_f32 v[4:5], v[96:97], v[6:7], v[4:5] op_sel_hi:[1,0,1]
	v_pk_fma_f32 v[2:3], v[90:91], v[6:7], v[2:3] op_sel:[0,1,0]
	v_pk_fma_f32 v[4:5], v[92:93], v[6:7], v[4:5] op_sel:[0,1,0]
	v_pk_fma_f32 v[2:3], v[86:87], v[8:9], v[2:3] op_sel_hi:[1,0,1]
	v_pk_fma_f32 v[4:5], v[88:89], v[8:9], v[4:5] op_sel_hi:[1,0,1]
	v_mov_b32_e32 v6, v9
	v_pk_fma_f32 v[4:5], v[84:85], v[6:7], v[4:5] op_sel_hi:[1,0,1]
	v_pk_fma_f32 v[2:3], v[82:83], v[6:7], v[2:3] op_sel_hi:[1,0,1]
	s_waitcnt lgkmcnt(0)
	v_pk_fma_f32 v[4:5], v[80:81], v[10:11], v[4:5] op_sel_hi:[1,0,1]
	v_pk_fma_f32 v[2:3], v[78:79], v[10:11], v[2:3] op_sel_hi:[1,0,1]
	v_pk_fma_f32 v[4:5], v[76:77], v[10:11], v[4:5] op_sel:[0,1,0]
	v_pk_fma_f32 v[2:3], v[74:75], v[10:11], v[2:3] op_sel:[0,1,0]
	v_pk_fma_f32 v[4:5], v[72:73], v[12:13], v[4:5] op_sel_hi:[1,0,1]
	v_pk_fma_f32 v[2:3], v[70:71], v[12:13], v[2:3] op_sel_hi:[1,0,1]
	v_mov_b32_e32 v6, v13
	v_pk_fma_f32 v[4:5], v[68:69], v[6:7], v[4:5] op_sel_hi:[1,0,1]
	v_pk_fma_f32 v[2:3], v[66:67], v[6:7], v[2:3] op_sel_hi:[1,0,1]
	v_pk_mul_f32 v[4:5], v[4:5], s[0:1] op_sel_hi:[1,0]
	v_pk_mul_f32 v[2:3], v[2:3], s[0:1] op_sel_hi:[1,0]
	v_add_co_u32_e32 v0, vcc, 0xf000, v0
	v_cvt_pk_f16_f32 v2, v2, v3
	v_cvt_pk_f16_f32 v3, v4, v5
	v_addc_co_u32_e32 v1, vcc, 0, v1, vcc
	global_store_dwordx2 v[0:1], v[2:3], off sc1
	s_endpgm

.LBB1_5:
	s_waitcnt lgkmcnt(0)
	s_waitcnt lgkmcnt(0)
	s_barrier
	s_setprio 1
	v_mfma_f32_16x16x32_f16 v[134:137], v[42:45], v[62:65], v[134:137]
	v_mfma_f32_16x16x32_f16 v[130:133], v[38:41], v[62:65], v[130:133]
	v_mfma_f32_16x16x32_f16 v[126:129], v[34:37], v[62:65], v[126:129]
	v_mfma_f32_16x16x32_f16 v[122:125], v[30:33], v[62:65], v[122:125]
	v_mfma_f32_16x16x32_f16 v[118:121], v[26:29], v[62:65], v[118:121]
	v_mfma_f32_16x16x32_f16 v[114:117], v[22:25], v[62:65], v[114:117]
	v_mfma_f32_16x16x32_f16 v[110:113], v[42:45], v[50:53], v[110:113]
	v_mfma_f32_16x16x32_f16 v[106:109], v[38:41], v[50:53], v[106:109]
	v_mfma_f32_16x16x32_f16 v[102:105], v[34:37], v[50:53], v[102:105]
	v_mfma_f32_16x16x32_f16 v[98:101], v[30:33], v[50:53], v[98:101]
	v_mfma_f32_16x16x32_f16 v[94:97], v[26:29], v[50:53], v[94:97]
	v_mfma_f32_16x16x32_f16 v[90:93], v[22:25], v[50:53], v[90:93]
	v_mfma_f32_16x16x32_f16 v[86:89], v[42:45], v[14:17], v[86:89]
	v_mfma_f32_16x16x32_f16 v[82:85], v[38:41], v[14:17], v[82:85]
	v_mfma_f32_16x16x32_f16 v[78:81], v[34:37], v[14:17], v[78:81]
	v_mfma_f32_16x16x32_f16 v[74:77], v[30:33], v[14:17], v[74:77]
	v_mfma_f32_16x16x32_f16 v[70:73], v[26:29], v[14:17], v[70:73]
	v_mfma_f32_16x16x32_f16 v[66:69], v[22:25], v[14:17], v[66:69]
	v_mfma_f32_16x16x32_f16 v[58:61], v[42:45], v[6:9], v[58:61]
	v_mfma_f32_16x16x32_f16 v[54:57], v[38:41], v[6:9], v[54:57]
	v_mfma_f32_16x16x32_f16 v[46:49], v[34:37], v[6:9], v[46:49]
	v_mfma_f32_16x16x32_f16 v[18:21], v[30:33], v[6:9], v[18:21]
	v_mfma_f32_16x16x32_f16 v[10:13], v[26:29], v[6:9], v[10:13]
	v_mfma_f32_16x16x32_f16 v[2:5], v[22:25], v[6:9], v[2:5]
	s_setprio 0
	s_barrier
	v_add_u32_e32 v6, s3, v1
	v_add_u32_e32 v22, s3, v152
	ds_read_b128 v[62:65], v6
	ds_read_b128 v[50:53], v6 offset:1024
	ds_read_b128 v[14:17], v6 offset:2048
	ds_read_b128 v[6:9], v6 offset:3072
	ds_read_b128 v[42:45], v22 offset:16384
	ds_read_b128 v[38:41], v22 offset:17408
	ds_read_b128 v[34:37], v22 offset:18432
	ds_read_b128 v[30:33], v22 offset:19456
	ds_read_b128 v[26:29], v22 offset:20480
	ds_read_b128 v[22:25], v22 offset:21504
	s_addk_i32 s3, 0x7000
	s_cmp_lg_u32 s3, 0x23000
	s_cselect_b32 s3, s3, 0
	s_add_i32 s2, s2, -1
	s_cmp_eq_u32 s2, 0
	s_cbranch_scc0 .LBB1_5
	s_waitcnt lgkmcnt(0)
	s_waitcnt lgkmcnt(0)
	s_barrier
	s_setprio 1
	v_mfma_f32_16x16x32_f16 v[134:137], v[42:45], v[62:65], v[134:137]
	v_mfma_f32_16x16x32_f16 v[130:133], v[38:41], v[62:65], v[130:133]
	v_mfma_f32_16x16x32_f16 v[126:129], v[34:37], v[62:65], v[126:129]
	v_mfma_f32_16x16x32_f16 v[122:125], v[30:33], v[62:65], v[122:125]
	v_mfma_f32_16x16x32_f16 v[118:121], v[26:29], v[62:65], v[118:121]
	v_mfma_f32_16x16x32_f16 v[114:117], v[22:25], v[62:65], v[114:117]
	v_mfma_f32_16x16x32_f16 v[110:113], v[42:45], v[50:53], v[110:113]
	v_mfma_f32_16x16x32_f16 v[106:109], v[38:41], v[50:53], v[106:109]
	v_mfma_f32_16x16x32_f16 v[102:105], v[34:37], v[50:53], v[102:105]
	v_mfma_f32_16x16x32_f16 v[98:101], v[30:33], v[50:53], v[98:101]
	v_mfma_f32_16x16x32_f16 v[94:97], v[26:29], v[50:53], v[94:97]
	v_mfma_f32_16x16x32_f16 v[90:93], v[22:25], v[50:53], v[90:93]
	v_mfma_f32_16x16x32_f16 v[86:89], v[42:45], v[14:17], v[86:89]
	v_mfma_f32_16x16x32_f16 v[82:85], v[38:41], v[14:17], v[82:85]
	v_mfma_f32_16x16x32_f16 v[78:81], v[34:37], v[14:17], v[78:81]
	v_mfma_f32_16x16x32_f16 v[74:77], v[30:33], v[14:17], v[74:77]
	v_mfma_f32_16x16x32_f16 v[62:65], v[26:29], v[14:17], v[70:73]
	v_mfma_f32_16x16x32_f16 v[50:53], v[22:25], v[14:17], v[66:69]
	v_mfma_f32_16x16x32_f16 v[42:45], v[42:45], v[6:9], v[58:61]
	v_mfma_f32_16x16x32_f16 v[38:41], v[38:41], v[6:9], v[54:57]
	v_mfma_f32_16x16x32_f16 v[34:37], v[34:37], v[6:9], v[46:49]
	v_mfma_f32_16x16x32_f16 v[14:17], v[30:33], v[6:9], v[18:21]
	v_mfma_f32_16x16x32_f16 v[10:13], v[26:29], v[6:9], v[10:13]
	v_mfma_f32_16x16x32_f16 v[2:5], v[22:25], v[6:9], v[2:5]
	s_setprio 0
	s_lshl_b32 s2, s17, 6
	s_or_b32 s2, s2, s18
	s_add_i32 s14, s16, s10
	s_cmpk_lt_i32 s14, 0x400
	s_cselect_b64 vcc, -1, 0
	s_ashr_i32 s12, s14, 10
	v_or_b32_e32 v7, s2, v153
	s_lshr_b32 s2, s2, 7
	s_ashr_i32 s13, s12, 31
	s_and_b32 s15, s2, 0xf0
	s_bfe_u32 s19, s14, 0x40006
	s_lshl_b64 s[12:13], s[12:13], 24
	s_add_u32 s20, s4, s12
	s_addc_u32 s21, s5, s13
	s_or_b32 s12, s15, s19
	s_lshl_b32 s12, s12, 18
	v_mov_b32_e32 v32, s7
	v_mov_b32_e32 v33, s6
	v_lshlrev_b32_e32 v7, 6, v7
	s_add_u32 s12, s20, s12
	v_lshlrev_b32_e32 v155, 3, v154
	v_cndmask_b32_e32 v6, v32, v33, vcc
	v_mov_b32_e32 v139, 0
	v_and_b32_e32 v142, 0x1f3c0, v7
	s_addc_u32 s13, s21, 0
	s_add_i32 s22, s14, 32
	v_pk_mul_f32 v[8:9], v[6:7], v[136:137] op_sel_hi:[0,1]
	v_pk_mul_f32 v[18:19], v[6:7], v[134:135] op_sel_hi:[0,1]
	v_pk_mul_f32 v[22:23], v[6:7], v[132:133] op_sel_hi:[0,1]
	v_pk_mul_f32 v[20:21], v[6:7], v[130:131] op_sel_hi:[0,1]
	v_and_or_b32 v144, s16, 32, v155
	v_lshlrev_b32_e32 v28, 1, v142
	v_mov_b32_e32 v29, v139
	s_cmpk_lt_i32 s14, 0x3e0
	v_cvt_pk_f16_f32 v18, v18, v19
	v_cvt_pk_f16_f32 v19, v8, v9
	v_cvt_pk_f16_f32 v20, v20, v21
	v_cvt_pk_f16_f32 v21, v22, v23
	v_lshl_add_u64 v[22:23], s[12:13], 0, v[28:29]
	v_lshlrev_b32_e32 v8, 1, v144
	v_mov_b32_e32 v9, v139
	s_cselect_b64 vcc, -1, 0
	s_ashr_i32 s12, s22, 10
	v_lshl_add_u64 v[22:23], v[22:23], 0, v[8:9]
	s_ashr_i32 s13, s12, 31
	global_store_dwordx4 v[22:23], v[18:21], off sc1
	s_bfe_u32 s23, s22, 0x40006
	s_lshl_b64 s[12:13], s[12:13], 24
	v_cndmask_b32_e32 v18, v32, v33, vcc
	v_pk_mul_f32 v[20:21], v[18:19], v[128:129] op_sel_hi:[0,1]
	v_pk_mul_f32 v[22:23], v[18:19], v[126:127] op_sel_hi:[0,1]
	v_pk_mul_f32 v[30:31], v[18:19], v[124:125] op_sel_hi:[0,1]
	v_pk_mul_f32 v[26:27], v[18:19], v[122:123] op_sel_hi:[0,1]
	v_and_or_b32 v19, s22, 32, v155
	s_add_u32 s22, s4, s12
	s_addc_u32 s24, s5, s13
	s_or_b32 s12, s15, s23
	s_lshl_b32 s12, s12, 18
	s_add_u32 s12, s22, s12
	s_addc_u32 s13, s24, 0
	s_add_i32 s25, s14, 64
	s_cmpk_lt_i32 s14, 0x3c0
	v_cvt_pk_f16_f32 v25, v20, v21
	v_lshl_add_u64 v[20:21], s[12:13], 0, v[28:29]
	s_cselect_b64 vcc, -1, 0
	s_ashr_i32 s12, s25, 10
	s_ashr_i32 s13, s12, 31
	s_bfe_u32 s25, s25, 0x40006
	s_lshl_b64 s[12:13], s[12:13], 24
	s_add_u32 s26, s4, s12
	s_addc_u32 s27, s5, s13
	s_or_b32 s12, s15, s25
	s_lshl_b32 s12, s12, 18
	v_cvt_pk_f16_f32 v24, v22, v23
	v_lshlrev_b32_e32 v22, 1, v19
	v_mov_b32_e32 v23, v139
	s_add_u32 s12, s26, s12
	s_mov_b32 s3, 0
	v_cvt_pk_f16_f32 v26, v26, v27
	v_cvt_pk_f16_f32 v27, v30, v31
	v_lshl_add_u64 v[20:21], v[20:21], 0, v[22:23]
	s_addc_u32 s13, s27, 0
	s_and_b32 s2, s2, 0xfffff0
	global_store_dwordx4 v[20:21], v[24:27], off sc1
	v_cndmask_b32_e32 v20, v32, v33, vcc
	v_lshl_add_u64 v[28:29], s[12:13], 0, v[28:29]
	s_or_b32 s12, s2, s19
	s_mov_b32 s13, s3
	v_pk_mul_f32 v[26:27], v[20:21], v[120:121] op_sel_hi:[0,1]
	v_pk_mul_f32 v[24:25], v[20:21], v[118:119] op_sel_hi:[0,1]
	v_pk_mul_f32 v[30:31], v[20:21], v[116:117] op_sel_hi:[0,1]
	v_pk_mul_f32 v[32:33], v[20:21], v[114:115] op_sel_hi:[0,1]
	s_lshl_b64 s[12:13], s[12:13], 18
	v_cvt_pk_f16_f32 v24, v24, v25
	v_cvt_pk_f16_f32 v25, v26, v27
	v_cvt_pk_f16_f32 v26, v32, v33
	v_cvt_pk_f16_f32 v27, v30, v31
	v_lshl_add_u64 v[28:29], v[28:29], 0, v[8:9]
	s_mov_b32 s28, 0x1ffc0
	v_mov_b32_e32 v19, 0x400
	s_add_u32 s12, s20, s12
	v_mov_b32_e32 v138, s15
	global_store_dwordx4 v[28:29], v[24:27], off sc1
	v_bitop3_b32 v146, v7, s28, v19 bitop3:0xc8
	v_pk_mul_f32 v[28:29], v[6:7], v[108:109] op_sel_hi:[0,1]
	v_pk_mul_f32 v[26:27], v[6:7], v[112:113] op_sel_hi:[0,1]
	v_pk_mul_f32 v[24:25], v[6:7], v[110:111] op_sel_hi:[0,1]
	s_addc_u32 s13, s21, s13
	s_or_b32 s14, s2, s23
	s_mov_b32 s15, s3
	v_pk_mul_f32 v[30:31], v[6:7], v[106:107] op_sel_hi:[0,1]
	v_cvt_pk_f16_f32 v24, v24, v25
	v_cvt_pk_f16_f32 v25, v26, v27
	v_cvt_pk_f16_f32 v27, v28, v29
	v_lshlrev_b32_e32 v28, 1, v146
	v_mov_b32_e32 v29, v139
	s_lshl_b64 s[14:15], s[14:15], 18
	v_cvt_pk_f16_f32 v26, v30, v31
	v_lshl_add_u64 v[30:31], s[12:13], 0, v[28:29]
	s_add_u32 s14, s22, s14
	v_mov_b64_e32 v[140:141], s[2:3]
	v_lshl_add_u64 v[30:31], v[30:31], 0, v[8:9]
	s_addc_u32 s15, s24, s15
	s_or_b32 s2, s2, s25
	global_store_dwordx4 v[30:31], v[24:27], off sc1
	v_pk_mul_f32 v[30:31], v[18:19], v[100:101] op_sel_hi:[0,1]
	s_lshl_b64 s[2:3], s[2:3], 18
	v_pk_mul_f32 v[26:27], v[18:19], v[104:105] op_sel_hi:[0,1]
	v_pk_mul_f32 v[24:25], v[18:19], v[102:103] op_sel_hi:[0,1]
	v_pk_mul_f32 v[32:33], v[18:19], v[98:99] op_sel_hi:[0,1]
	v_cvt_pk_f16_f32 v24, v24, v25
	v_cvt_pk_f16_f32 v25, v26, v27
	v_cvt_pk_f16_f32 v27, v30, v31
	v_lshl_add_u64 v[30:31], s[14:15], 0, v[28:29]
	s_add_u32 s2, s26, s2
	v_cvt_pk_f16_f32 v26, v32, v33
	v_lshl_add_u64 v[30:31], v[30:31], 0, v[22:23]
	s_addc_u32 s3, s27, s3
	global_store_dwordx4 v[30:31], v[24:27], off sc1
	v_pk_mul_f32 v[30:31], v[20:21], v[92:93] op_sel_hi:[0,1]
	v_pk_mul_f32 v[32:33], v[20:21], v[90:91] op_sel_hi:[0,1]
	v_pk_mul_f32 v[26:27], v[20:21], v[96:97] op_sel_hi:[0,1]
	v_pk_mul_f32 v[24:25], v[20:21], v[94:95] op_sel_hi:[0,1]
	v_lshl_add_u64 v[28:29], s[2:3], 0, v[28:29]
	v_cvt_pk_f16_f32 v24, v24, v25
	v_cvt_pk_f16_f32 v25, v26, v27
	v_cvt_pk_f16_f32 v26, v32, v33
	v_cvt_pk_f16_f32 v27, v30, v31
	v_lshl_add_u64 v[28:29], v[28:29], 0, v[8:9]
	v_mov_b32_e32 v19, 0x800
	global_store_dwordx4 v[28:29], v[24:27], off sc1
	v_bitop3_b32 v148, v7, s28, v19 bitop3:0xc8
	v_pk_mul_f32 v[28:29], v[6:7], v[84:85] op_sel_hi:[0,1]
	v_pk_mul_f32 v[26:27], v[6:7], v[88:89] op_sel_hi:[0,1]
	v_pk_mul_f32 v[24:25], v[6:7], v[86:87] op_sel_hi:[0,1]
	v_pk_mul_f32 v[30:31], v[6:7], v[82:83] op_sel_hi:[0,1]
	v_cvt_pk_f16_f32 v24, v24, v25
	v_cvt_pk_f16_f32 v25, v26, v27
	v_cvt_pk_f16_f32 v27, v28, v29
	v_lshlrev_b32_e32 v28, 1, v148
	v_mov_b32_e32 v29, v139
	v_cvt_pk_f16_f32 v26, v30, v31
	v_lshl_add_u64 v[30:31], s[12:13], 0, v[28:29]
	v_lshl_add_u64 v[30:31], v[30:31], 0, v[8:9]
	global_store_dwordx4 v[30:31], v[24:27], off sc1
	v_pk_mul_f32 v[30:31], v[18:19], v[76:77] op_sel_hi:[0,1]
	v_pk_mul_f32 v[32:33], v[18:19], v[74:75] op_sel_hi:[0,1]
	v_pk_mul_f32 v[26:27], v[18:19], v[80:81] op_sel_hi:[0,1]
	v_pk_mul_f32 v[24:25], v[18:19], v[78:79] op_sel_hi:[0,1]
	v_cvt_pk_f16_f32 v24, v24, v25
	v_cvt_pk_f16_f32 v25, v26, v27
	v_cvt_pk_f16_f32 v27, v30, v31
	v_lshl_add_u64 v[30:31], s[14:15], 0, v[28:29]
	v_cvt_pk_f16_f32 v26, v32, v33
	v_lshl_add_u64 v[30:31], v[30:31], 0, v[22:23]
	global_store_dwordx4 v[30:31], v[24:27], off sc1
	v_pk_mul_f32 v[30:31], v[20:21], v[52:53] op_sel_hi:[0,1]
	v_pk_mul_f32 v[32:33], v[20:21], v[50:51] op_sel_hi:[0,1]
	v_pk_mul_f32 v[26:27], v[20:21], v[64:65] op_sel_hi:[0,1]
	v_pk_mul_f32 v[24:25], v[20:21], v[62:63] op_sel_hi:[0,1]
	v_lshl_add_u64 v[28:29], s[2:3], 0, v[28:29]
	v_cvt_pk_f16_f32 v24, v24, v25
	v_cvt_pk_f16_f32 v25, v26, v27
	v_cvt_pk_f16_f32 v26, v32, v33
	v_cvt_pk_f16_f32 v27, v30, v31
	v_lshl_add_u64 v[28:29], v[28:29], 0, v[8:9]
	v_mov_b32_e32 v19, 0xc00
	global_store_dwordx4 v[28:29], v[24:27], off sc1
	v_bitop3_b32 v150, v7, s28, v19 bitop3:0xc8
	v_pk_mul_f32 v[28:29], v[6:7], v[40:41] op_sel_hi:[0,1]
	v_pk_mul_f32 v[26:27], v[6:7], v[44:45] op_sel_hi:[0,1]
	v_pk_mul_f32 v[24:25], v[6:7], v[42:43] op_sel_hi:[0,1]
	v_pk_mul_f32 v[6:7], v[6:7], v[38:39] op_sel_hi:[0,1]
	v_cvt_pk_f16_f32 v24, v24, v25
	v_cvt_pk_f16_f32 v25, v26, v27
	v_cvt_pk_f16_f32 v26, v6, v7
	v_lshlrev_b32_e32 v6, 1, v150
	v_mov_b32_e32 v7, v139
	v_cvt_pk_f16_f32 v27, v28, v29
	v_lshl_add_u64 v[28:29], s[12:13], 0, v[6:7]
	v_lshl_add_u64 v[28:29], v[28:29], 0, v[8:9]
	global_store_dwordx4 v[28:29], v[24:27], off sc1
	v_pk_mul_f32 v[28:29], v[18:19], v[16:17] op_sel_hi:[0,1]
	v_pk_mul_f32 v[16:17], v[18:19], v[14:15] op_sel_hi:[0,1]
	v_pk_mul_f32 v[24:25], v[18:19], v[36:37] op_sel_hi:[0,1]
	v_pk_mul_f32 v[26:27], v[18:19], v[34:35] op_sel_hi:[0,1]
	v_lshl_add_u64 v[18:19], s[14:15], 0, v[6:7]
	v_cvt_pk_f16_f32 v14, v26, v27
	v_cvt_pk_f16_f32 v15, v24, v25
	v_cvt_pk_f16_f32 v16, v16, v17
	v_cvt_pk_f16_f32 v17, v28, v29
	v_lshl_add_u64 v[18:19], v[18:19], 0, v[22:23]
	global_store_dwordx4 v[18:19], v[14:17], off sc1
	v_pk_mul_f32 v[12:13], v[20:21], v[12:13] op_sel_hi:[0,1]
	v_pk_mul_f32 v[10:11], v[20:21], v[10:11] op_sel_hi:[0,1]
	v_pk_mul_f32 v[14:15], v[20:21], v[4:5] op_sel_hi:[0,1]
	v_pk_mul_f32 v[4:5], v[20:21], v[2:3] op_sel_hi:[0,1]
	v_lshl_add_u64 v[6:7], s[2:3], 0, v[6:7]
	v_mov_b32_e32 v143, v139
	v_mov_b32_e32 v145, v139
	v_mov_b32_e32 v147, v139
	v_mov_b32_e32 v149, v139
	v_mov_b32_e32 v151, v139
	v_cvt_pk_f16_f32 v2, v10, v11
	v_cvt_pk_f16_f32 v3, v12, v13
	v_cvt_pk_f16_f32 v4, v4, v5
	v_cvt_pk_f16_f32 v5, v14, v15
	v_lshl_add_u64 v[6:7], v[6:7], 0, v[8:9]
	global_store_dwordx4 v[6:7], v[2:5], off sc1
	s_barrier
	ds_read_b128 v[22:25], v1 offset:57344
	ds_read_b128 v[18:21], v1 offset:58368
	ds_read_b128 v[6:9], v1 offset:59392
	ds_read_b128 v[2:5], v1 offset:60416
	v_or_b32_e32 v10, 0x12000, v152
	v_add_u32_e32 v11, 0x12400, v152
	v_add_u32_e32 v26, 0x12800, v152
	ds_read_b128 v[14:17], v10
	ds_read_b128 v[10:13], v11
	v_add_u32_e32 v27, 0x12c00, v152
	ds_read_b128 v[110:113], v26
	ds_read_b128 v[106:109], v27
	v_add_u32_e32 v26, 0x13000, v152
	v_add_u32_e32 v27, 0x13400, v152
	ds_read_b128 v[122:125], v26
	ds_read_b128 v[118:121], v27
	s_mov_b32 s3, 0x15000
	s_mov_b32 s2, 31
	v_mov_b32_e32 v98, v139
	v_mov_b32_e32 v99, v139
	v_mov_b32_e32 v100, v139
	v_mov_b32_e32 v101, v139
	v_mov_b32_e32 v102, v139
	v_mov_b32_e32 v103, v139
	v_mov_b32_e32 v104, v139
	v_mov_b32_e32 v105, v139
	v_mov_b32_e32 v114, v139
	v_mov_b32_e32 v115, v139
	v_mov_b32_e32 v116, v139
	v_mov_b32_e32 v117, v139
	v_mov_b32_e32 v126, v139
	v_mov_b32_e32 v127, v139
	v_mov_b32_e32 v128, v139
	v_mov_b32_e32 v129, v139
	v_mov_b32_e32 v130, v139
	v_mov_b32_e32 v131, v139
	v_mov_b32_e32 v132, v139
	v_mov_b32_e32 v133, v139
	v_mov_b32_e32 v134, v139
	v_mov_b32_e32 v135, v139
	v_mov_b32_e32 v136, v139
	v_mov_b32_e32 v137, v139
	v_mov_b32_e32 v26, v139
	v_mov_b32_e32 v27, v139
	v_mov_b32_e32 v28, v139
	v_mov_b32_e32 v29, v139
	v_mov_b32_e32 v30, v139
	v_mov_b32_e32 v31, v139
	v_mov_b32_e32 v32, v139
	v_mov_b32_e32 v33, v139
	v_mov_b32_e32 v34, v139
	v_mov_b32_e32 v35, v139
	v_mov_b32_e32 v36, v139
	v_mov_b32_e32 v37, v139
	v_mov_b32_e32 v38, v139
	v_mov_b32_e32 v39, v139
	v_mov_b32_e32 v40, v139
	v_mov_b32_e32 v41, v139
	v_mov_b32_e32 v42, v139
	v_mov_b32_e32 v43, v139
	v_mov_b32_e32 v44, v139
	v_mov_b32_e32 v45, v139
	v_mov_b32_e32 v46, v139
	v_mov_b32_e32 v47, v139
	v_mov_b32_e32 v48, v139
	v_mov_b32_e32 v49, v139
	v_mov_b32_e32 v50, v139
	v_mov_b32_e32 v51, v139
	v_mov_b32_e32 v52, v139
	v_mov_b32_e32 v53, v139
	v_mov_b32_e32 v54, v139
	v_mov_b32_e32 v55, v139
	v_mov_b32_e32 v56, v139
	v_mov_b32_e32 v57, v139
	v_mov_b32_e32 v58, v139
	v_mov_b32_e32 v59, v139
	v_mov_b32_e32 v60, v139
	v_mov_b32_e32 v61, v139
	v_mov_b32_e32 v62, v139
	v_mov_b32_e32 v63, v139
	v_mov_b32_e32 v64, v139
	v_mov_b32_e32 v65, v139
	v_mov_b32_e32 v66, v139
	v_mov_b32_e32 v67, v139
	v_mov_b32_e32 v68, v139
	v_mov_b32_e32 v69, v139
	v_mov_b32_e32 v70, v139
	v_mov_b32_e32 v71, v139
	v_mov_b32_e32 v72, v139
	v_mov_b32_e32 v73, v139
	v_mov_b32_e32 v74, v139
	v_mov_b32_e32 v75, v139
	v_mov_b32_e32 v76, v139
	v_mov_b32_e32 v77, v139
	v_mov_b32_e32 v78, v139
	v_mov_b32_e32 v79, v139
	v_mov_b32_e32 v80, v139
	v_mov_b32_e32 v81, v139
	v_mov_b32_e32 v82, v139
	v_mov_b32_e32 v83, v139
	v_mov_b32_e32 v84, v139
	v_mov_b32_e32 v85, v139
	v_mov_b32_e32 v86, v139
	v_mov_b32_e32 v87, v139
	v_mov_b32_e32 v88, v139
	v_mov_b32_e32 v89, v139
	v_mov_b32_e32 v90, v139
	v_mov_b32_e32 v91, v139
	v_mov_b32_e32 v92, v139
	v_mov_b32_e32 v93, v139
	v_mov_b32_e32 v94, v139
	v_mov_b32_e32 v95, v139
	v_mov_b32_e32 v96, v139
	v_mov_b32_e32 v97, v139

.LBB1_11:
	s_waitcnt lgkmcnt(0)
	s_waitcnt lgkmcnt(0)
	s_barrier
	v_add_u32_e32 v110, s3, v1
	v_add_u32_e32 v134, s3, v152
	ds_read_b128 v[98:101], v110
	ds_read_b128 v[102:105], v110 offset:1024
	ds_read_b128 v[106:109], v110 offset:2048
	ds_read_b128 v[110:113], v110 offset:3072
	ds_read_b128 v[114:117], v134 offset:16384
	ds_read_b128 v[118:121], v134 offset:17408
	ds_read_b128 v[122:125], v134 offset:18432
	ds_read_b128 v[126:129], v134 offset:19456
	ds_read_b128 v[130:133], v134 offset:20480
	ds_read_b128 v[134:137], v134 offset:21504
	s_addk_i32 s3, 0x7000
	s_barrier
	s_setprio 1
	s_waitcnt lgkmcnt(5)
	v_mfma_f32_16x16x32_f16 v[94:97], v[114:117], v[98:101], v[94:97]
	s_cmp_lg_u32 s3, 0x23000
	s_cselect_b32 s3, s3, 0
	s_waitcnt lgkmcnt(4)
	v_mfma_f32_16x16x32_f16 v[90:93], v[118:121], v[98:101], v[90:93]
	s_waitcnt lgkmcnt(3)
	v_mfma_f32_16x16x32_f16 v[86:89], v[122:125], v[98:101], v[86:89]
	s_waitcnt lgkmcnt(2)
	v_mfma_f32_16x16x32_f16 v[82:85], v[126:129], v[98:101], v[82:85]
	s_waitcnt lgkmcnt(1)
	v_mfma_f32_16x16x32_f16 v[78:81], v[130:133], v[98:101], v[78:81]
	s_waitcnt lgkmcnt(0)
	v_mfma_f32_16x16x32_f16 v[74:77], v[134:137], v[98:101], v[74:77]
	v_mfma_f32_16x16x32_f16 v[70:73], v[114:117], v[102:105], v[70:73]
	v_mfma_f32_16x16x32_f16 v[66:69], v[118:121], v[102:105], v[66:69]
	v_mfma_f32_16x16x32_f16 v[62:65], v[122:125], v[102:105], v[62:65]
	v_mfma_f32_16x16x32_f16 v[58:61], v[126:129], v[102:105], v[58:61]
	v_mfma_f32_16x16x32_f16 v[54:57], v[130:133], v[102:105], v[54:57]
	v_mfma_f32_16x16x32_f16 v[50:53], v[134:137], v[102:105], v[50:53]
	v_mfma_f32_16x16x32_f16 v[46:49], v[114:117], v[106:109], v[46:49]
	v_mfma_f32_16x16x32_f16 v[42:45], v[118:121], v[106:109], v[42:45]
	v_mfma_f32_16x16x32_f16 v[38:41], v[122:125], v[106:109], v[38:41]
	v_mfma_f32_16x16x32_f16 v[34:37], v[126:129], v[106:109], v[34:37]
	v_mfma_f32_16x16x32_f16 v[30:33], v[130:133], v[106:109], v[30:33]
	v_mfma_f32_16x16x32_f16 v[26:29], v[134:137], v[106:109], v[26:29]
	v_mfma_f32_16x16x32_f16 v[22:25], v[114:117], v[110:113], v[22:25]
	v_mfma_f32_16x16x32_f16 v[18:21], v[118:121], v[110:113], v[18:21]
	v_mfma_f32_16x16x32_f16 v[14:17], v[122:125], v[110:113], v[14:17]
	v_mfma_f32_16x16x32_f16 v[10:13], v[126:129], v[110:113], v[10:13]
	v_mfma_f32_16x16x32_f16 v[6:9], v[130:133], v[110:113], v[6:9]
	v_mfma_f32_16x16x32_f16 v[2:5], v[134:137], v[110:113], v[2:5]
	s_setprio 0
	s_waitcnt lgkmcnt(0)
	s_waitcnt lgkmcnt(0)
	s_barrier
	v_add_u32_e32 v110, s3, v1
	v_add_u32_e32 v134, s3, v152
	ds_read_b128 v[98:101], v110
	ds_read_b128 v[102:105], v110 offset:1024
	ds_read_b128 v[106:109], v110 offset:2048
	ds_read_b128 v[110:113], v110 offset:3072
	ds_read_b128 v[114:117], v134 offset:16384
	ds_read_b128 v[118:121], v134 offset:17408
	ds_read_b128 v[122:125], v134 offset:18432
	ds_read_b128 v[126:129], v134 offset:19456
	ds_read_b128 v[130:133], v134 offset:20480
	ds_read_b128 v[134:137], v134 offset:21504
	s_addk_i32 s3, 0x7000
	s_barrier
	s_setprio 1
	s_waitcnt lgkmcnt(5)
	v_mfma_f32_16x16x32_f16 v[94:97], v[114:117], v[98:101], v[94:97]
	s_cmp_lg_u32 s3, 0x23000
	s_cselect_b32 s3, s3, 0
	s_waitcnt lgkmcnt(4)
	v_mfma_f32_16x16x32_f16 v[90:93], v[118:121], v[98:101], v[90:93]
	s_waitcnt lgkmcnt(3)
	v_mfma_f32_16x16x32_f16 v[86:89], v[122:125], v[98:101], v[86:89]
	s_waitcnt lgkmcnt(2)
	v_mfma_f32_16x16x32_f16 v[82:85], v[126:129], v[98:101], v[82:85]
	s_waitcnt lgkmcnt(1)
	v_mfma_f32_16x16x32_f16 v[78:81], v[130:133], v[98:101], v[78:81]
	s_waitcnt lgkmcnt(0)
	v_mfma_f32_16x16x32_f16 v[74:77], v[134:137], v[98:101], v[74:77]
	v_mfma_f32_16x16x32_f16 v[70:73], v[114:117], v[102:105], v[70:73]
	v_mfma_f32_16x16x32_f16 v[66:69], v[118:121], v[102:105], v[66:69]
	v_mfma_f32_16x16x32_f16 v[62:65], v[122:125], v[102:105], v[62:65]
	v_mfma_f32_16x16x32_f16 v[58:61], v[126:129], v[102:105], v[58:61]
	v_mfma_f32_16x16x32_f16 v[54:57], v[130:133], v[102:105], v[54:57]
	v_mfma_f32_16x16x32_f16 v[50:53], v[134:137], v[102:105], v[50:53]
	v_mfma_f32_16x16x32_f16 v[46:49], v[114:117], v[106:109], v[46:49]
	v_mfma_f32_16x16x32_f16 v[42:45], v[118:121], v[106:109], v[42:45]
	v_mfma_f32_16x16x32_f16 v[38:41], v[122:125], v[106:109], v[38:41]
	v_mfma_f32_16x16x32_f16 v[34:37], v[126:129], v[106:109], v[34:37]
	v_mfma_f32_16x16x32_f16 v[30:33], v[130:133], v[106:109], v[30:33]
	v_mfma_f32_16x16x32_f16 v[26:29], v[134:137], v[106:109], v[26:29]
	v_mfma_f32_16x16x32_f16 v[22:25], v[114:117], v[110:113], v[22:25]
	v_mfma_f32_16x16x32_f16 v[18:21], v[118:121], v[110:113], v[18:21]
	v_mfma_f32_16x16x32_f16 v[14:17], v[122:125], v[110:113], v[14:17]
	v_mfma_f32_16x16x32_f16 v[10:13], v[126:129], v[110:113], v[10:13]
	v_mfma_f32_16x16x32_f16 v[6:9], v[130:133], v[110:113], v[6:9]
	v_mfma_f32_16x16x32_f16 v[2:5], v[134:137], v[110:113], v[2:5]
	s_setprio 0
	s_add_i32 s2, s2, -2
	s_cmp_eq_u32 s2, 0
	s_cbranch_scc0 .LBB1_11
	s_lshl_b32 s2, s17, 6
	s_or_b32 s2, s2, s18
	s_add_i32 s14, s16, s10
	s_cmpk_lt_i32 s14, 0x400
	s_cselect_b64 vcc, -1, 0
	s_ashr_i32 s12, s14, 10
	v_or_b32_e32 v99, s2, v153
	s_lshr_b32 s2, s2, 7
	s_ashr_i32 s13, s12, 31
	s_and_b32 s15, s2, 0xf0
	s_bfe_u32 s18, s14, 0x40006
	s_lshl_b64 s[12:13], s[12:13], 24
	s_add_u32 s19, s4, s12
	v_mov_b32_e32 v102, s7
	v_mov_b32_e32 v103, s6
	s_addc_u32 s20, s5, s13
	s_or_b32 s12, s15, s18
	v_cndmask_b32_e32 v98, v102, v103, vcc
	v_lshlrev_b32_e32 v99, 6, v99
	s_lshl_b32 s12, s12, 18
	v_lshlrev_b32_e32 v155, 3, v154
	v_mov_b32_e32 v139, 0
	v_and_b32_e32 v142, 0x1f3c0, v99
	v_pk_mul_f32 v[96:97], v[98:99], v[96:97] op_sel_hi:[0,1]
	s_add_u32 s12, s19, s12
	v_pk_mul_f32 v[94:95], v[98:99], v[94:95] op_sel_hi:[0,1]
	v_pk_mul_f32 v[100:101], v[98:99], v[92:93] op_sel_hi:[0,1]
	v_pk_mul_f32 v[90:91], v[98:99], v[90:91] op_sel_hi:[0,1]
	v_cvt_pk_f16_f32 v93, v96, v97
	v_and_or_b32 v144, s16, 32, v155
	s_addc_u32 s13, s20, 0
	v_lshlrev_b32_e32 v96, 1, v142
	v_mov_b32_e32 v97, v139
	s_add_i32 s21, s14, 32
	v_cvt_pk_f16_f32 v92, v94, v95
	v_cvt_pk_f16_f32 v94, v90, v91
	v_cvt_pk_f16_f32 v95, v100, v101
	v_lshl_add_u64 v[100:101], s[12:13], 0, v[96:97]
	v_lshlrev_b32_e32 v90, 1, v144
	v_mov_b32_e32 v91, v139
	s_cmpk_lt_i32 s14, 0x3e0
	v_lshl_add_u64 v[100:101], v[100:101], 0, v[90:91]
	s_cselect_b64 vcc, -1, 0
	s_ashr_i32 s12, s21, 10
	global_store_dwordx4 v[100:101], v[92:95], off sc1
	s_ashr_i32 s13, s12, 31
	s_bfe_u32 s22, s21, 0x40006
	v_cndmask_b32_e32 v92, v102, v103, vcc
	v_pk_mul_f32 v[88:89], v[92:93], v[88:89] op_sel_hi:[0,1]
	v_pk_mul_f32 v[86:87], v[92:93], v[86:87] op_sel_hi:[0,1]
	v_pk_mul_f32 v[84:85], v[92:93], v[84:85] op_sel_hi:[0,1]
	s_lshl_b64 s[12:13], s[12:13], 24
	v_cvt_pk_f16_f32 v86, v86, v87
	v_cvt_pk_f16_f32 v87, v88, v89
	v_cvt_pk_f16_f32 v89, v84, v85
	v_and_or_b32 v84, s21, 32, v155
	s_add_u32 s21, s4, s12
	s_addc_u32 s23, s5, s13
	s_or_b32 s12, s15, s22
	s_lshl_b32 s12, s12, 18
	s_add_u32 s12, s21, s12
	s_addc_u32 s13, s23, 0
	s_add_i32 s24, s14, 64
	v_pk_mul_f32 v[82:83], v[92:93], v[82:83] op_sel_hi:[0,1]
	s_cmpk_lt_i32 s14, 0x3c0
	v_cvt_pk_f16_f32 v88, v82, v83
	v_lshl_add_u64 v[82:83], s[12:13], 0, v[96:97]
	s_cselect_b64 vcc, -1, 0
	s_ashr_i32 s12, s24, 10
	s_ashr_i32 s13, s12, 31
	s_bfe_u32 s24, s24, 0x40006
	s_lshl_b64 s[12:13], s[12:13], 24
	s_add_u32 s25, s4, s12
	v_lshlrev_b32_e32 v84, 1, v84
	v_mov_b32_e32 v85, v139
	s_addc_u32 s26, s5, s13
	s_or_b32 s12, s15, s24
	v_lshl_add_u64 v[82:83], v[82:83], 0, v[84:85]
	s_lshl_b32 s12, s12, 18
	global_store_dwordx4 v[82:83], v[86:89], off sc1
	v_cndmask_b32_e32 v82, v102, v103, vcc
	s_add_u32 s12, s25, s12
	s_mov_b32 s3, 0
	v_pk_mul_f32 v[78:79], v[82:83], v[78:79] op_sel_hi:[0,1]
	s_addc_u32 s13, s26, 0
	s_and_b32 s2, s2, 0xfffff0
	v_pk_mul_f32 v[86:87], v[82:83], v[76:77] op_sel_hi:[0,1]
	v_pk_mul_f32 v[76:77], v[82:83], v[74:75] op_sel_hi:[0,1]
	v_cvt_pk_f16_f32 v74, v78, v79
	v_lshl_add_u64 v[78:79], s[12:13], 0, v[96:97]
	s_or_b32 s12, s2, s18
	s_mov_b32 s13, s3
	v_pk_mul_f32 v[80:81], v[82:83], v[80:81] op_sel_hi:[0,1]
	s_lshl_b64 s[12:13], s[12:13], 18
	v_cvt_pk_f16_f32 v75, v80, v81
	v_cvt_pk_f16_f32 v76, v76, v77
	v_cvt_pk_f16_f32 v77, v86, v87
	v_lshl_add_u64 v[78:79], v[78:79], 0, v[90:91]
	s_add_u32 s12, s19, s12
	v_mov_b32_e32 v138, s15
	global_store_dwordx4 v[78:79], v[74:77], off sc1
	s_mov_b32 s27, 0x1ffc0
	s_addc_u32 s13, s20, s13
	v_mov_b32_e32 v74, 0x400
	s_or_b32 s14, s2, s22
	s_mov_b32 s15, s3
	v_bitop3_b32 v146, v99, s27, v74 bitop3:0xc8
	v_pk_mul_f32 v[70:71], v[98:99], v[70:71] op_sel_hi:[0,1]
	s_lshl_b64 s[14:15], s[14:15], 18
	v_pk_mul_f32 v[72:73], v[98:99], v[72:73] op_sel_hi:[0,1]
	v_pk_mul_f32 v[74:75], v[98:99], v[68:69] op_sel_hi:[0,1]
	v_pk_mul_f32 v[68:69], v[98:99], v[66:67] op_sel_hi:[0,1]
	v_cvt_pk_f16_f32 v66, v70, v71
	v_lshlrev_b32_e32 v70, 1, v146
	v_mov_b32_e32 v71, v139
	s_add_u32 s14, s21, s14
	v_mov_b64_e32 v[140:141], s[2:3]
	v_cvt_pk_f16_f32 v67, v72, v73
	v_lshl_add_u64 v[72:73], s[12:13], 0, v[70:71]
	s_addc_u32 s15, s23, s15
	s_or_b32 s2, s2, s24
	v_cvt_pk_f16_f32 v68, v68, v69
	v_cvt_pk_f16_f32 v69, v74, v75
	v_lshl_add_u64 v[72:73], v[72:73], 0, v[90:91]
	v_pk_mul_f32 v[62:63], v[92:93], v[62:63] op_sel_hi:[0,1]
	s_lshl_b64 s[2:3], s[2:3], 18
	global_store_dwordx4 v[72:73], v[66:69], off sc1
	v_pk_mul_f32 v[64:65], v[92:93], v[64:65] op_sel_hi:[0,1]
	s_add_u32 s2, s25, s2
	v_pk_mul_f32 v[66:67], v[92:93], v[60:61] op_sel_hi:[0,1]
	v_pk_mul_f32 v[60:61], v[92:93], v[58:59] op_sel_hi:[0,1]
	v_cvt_pk_f16_f32 v58, v62, v63
	v_lshl_add_u64 v[62:63], s[14:15], 0, v[70:71]
	v_cvt_pk_f16_f32 v59, v64, v65
	v_cvt_pk_f16_f32 v60, v60, v61
	v_cvt_pk_f16_f32 v61, v66, v67
	v_lshl_add_u64 v[62:63], v[62:63], 0, v[84:85]
	v_pk_mul_f32 v[54:55], v[82:83], v[54:55] op_sel_hi:[0,1]
	s_addc_u32 s3, s26, s3
	global_store_dwordx4 v[62:63], v[58:61], off sc1
	v_pk_mul_f32 v[56:57], v[82:83], v[56:57] op_sel_hi:[0,1]
	v_pk_mul_f32 v[46:47], v[98:99], v[46:47] op_sel_hi:[0,1]
	v_pk_mul_f32 v[58:59], v[82:83], v[52:53] op_sel_hi:[0,1]
	v_pk_mul_f32 v[52:53], v[82:83], v[50:51] op_sel_hi:[0,1]
	v_cvt_pk_f16_f32 v50, v54, v55
	v_lshl_add_u64 v[54:55], s[2:3], 0, v[70:71]
	v_cvt_pk_f16_f32 v51, v56, v57
	v_cvt_pk_f16_f32 v52, v52, v53
	v_cvt_pk_f16_f32 v53, v58, v59
	v_lshl_add_u64 v[54:55], v[54:55], 0, v[90:91]
	global_store_dwordx4 v[54:55], v[50:53], off sc1
	v_pk_mul_f32 v[48:49], v[98:99], v[48:49] op_sel_hi:[0,1]
	v_pk_mul_f32 v[38:39], v[92:93], v[38:39] op_sel_hi:[0,1]
	v_mov_b32_e32 v50, 0x800
	v_bitop3_b32 v148, v99, s27, v50 bitop3:0xc8
	v_pk_mul_f32 v[50:51], v[98:99], v[44:45] op_sel_hi:[0,1]
	v_pk_mul_f32 v[44:45], v[98:99], v[42:43] op_sel_hi:[0,1]
	v_cvt_pk_f16_f32 v42, v46, v47
	v_lshlrev_b32_e32 v46, 1, v148
	v_mov_b32_e32 v47, v139
	v_cvt_pk_f16_f32 v43, v48, v49
	v_lshl_add_u64 v[48:49], s[12:13], 0, v[46:47]
	v_cvt_pk_f16_f32 v44, v44, v45
	v_cvt_pk_f16_f32 v45, v50, v51
	v_lshl_add_u64 v[48:49], v[48:49], 0, v[90:91]
	global_store_dwordx4 v[48:49], v[42:45], off sc1
	v_pk_mul_f32 v[40:41], v[92:93], v[40:41] op_sel_hi:[0,1]
	v_pk_mul_f32 v[30:31], v[82:83], v[30:31] op_sel_hi:[0,1]
	v_pk_mul_f32 v[42:43], v[92:93], v[36:37] op_sel_hi:[0,1]
	v_pk_mul_f32 v[36:37], v[92:93], v[34:35] op_sel_hi:[0,1]
	v_cvt_pk_f16_f32 v34, v38, v39
	v_lshl_add_u64 v[38:39], s[14:15], 0, v[46:47]
	v_cvt_pk_f16_f32 v35, v40, v41
	v_cvt_pk_f16_f32 v36, v36, v37
	v_cvt_pk_f16_f32 v37, v42, v43
	v_lshl_add_u64 v[38:39], v[38:39], 0, v[84:85]
	global_store_dwordx4 v[38:39], v[34:37], off sc1
	v_pk_mul_f32 v[32:33], v[82:83], v[32:33] op_sel_hi:[0,1]
	v_pk_mul_f32 v[22:23], v[98:99], v[22:23] op_sel_hi:[0,1]
	v_pk_mul_f32 v[34:35], v[82:83], v[28:29] op_sel_hi:[0,1]
	v_pk_mul_f32 v[28:29], v[82:83], v[26:27] op_sel_hi:[0,1]
	v_cvt_pk_f16_f32 v26, v30, v31
	v_lshl_add_u64 v[30:31], s[2:3], 0, v[46:47]
	v_cvt_pk_f16_f32 v27, v32, v33
	v_cvt_pk_f16_f32 v28, v28, v29
	v_cvt_pk_f16_f32 v29, v34, v35
	v_lshl_add_u64 v[30:31], v[30:31], 0, v[90:91]
	global_store_dwordx4 v[30:31], v[26:29], off sc1
	v_pk_mul_f32 v[24:25], v[98:99], v[24:25] op_sel_hi:[0,1]
	v_pk_mul_f32 v[14:15], v[92:93], v[14:15] op_sel_hi:[0,1]
	v_mov_b32_e32 v26, 0xc00
	v_bitop3_b32 v150, v99, s27, v26 bitop3:0xc8
	v_pk_mul_f32 v[26:27], v[98:99], v[20:21] op_sel_hi:[0,1]
	v_pk_mul_f32 v[20:21], v[98:99], v[18:19] op_sel_hi:[0,1]
	v_cvt_pk_f16_f32 v18, v22, v23
	v_lshlrev_b32_e32 v22, 1, v150
	v_mov_b32_e32 v23, v139
	v_cvt_pk_f16_f32 v19, v24, v25
	v_lshl_add_u64 v[24:25], s[12:13], 0, v[22:23]
	v_cvt_pk_f16_f32 v20, v20, v21
	v_cvt_pk_f16_f32 v21, v26, v27
	v_lshl_add_u64 v[24:25], v[24:25], 0, v[90:91]
	global_store_dwordx4 v[24:25], v[18:21], off sc1
	v_pk_mul_f32 v[16:17], v[92:93], v[16:17] op_sel_hi:[0,1]
	v_pk_mul_f32 v[6:7], v[82:83], v[6:7] op_sel_hi:[0,1]
	v_pk_mul_f32 v[18:19], v[92:93], v[12:13] op_sel_hi:[0,1]
	v_pk_mul_f32 v[12:13], v[92:93], v[10:11] op_sel_hi:[0,1]
	v_cvt_pk_f16_f32 v10, v14, v15
	v_lshl_add_u64 v[14:15], s[14:15], 0, v[22:23]
	v_cvt_pk_f16_f32 v11, v16, v17
	v_cvt_pk_f16_f32 v12, v12, v13
	v_cvt_pk_f16_f32 v13, v18, v19
	v_lshl_add_u64 v[14:15], v[14:15], 0, v[84:85]
	global_store_dwordx4 v[14:15], v[10:13], off sc1
	v_pk_mul_f32 v[8:9], v[82:83], v[8:9] op_sel_hi:[0,1]
	v_mov_b32_e32 v143, v139
	v_pk_mul_f32 v[10:11], v[82:83], v[4:5] op_sel_hi:[0,1]
	v_pk_mul_f32 v[4:5], v[82:83], v[2:3] op_sel_hi:[0,1]
	v_cvt_pk_f16_f32 v2, v6, v7
	v_lshl_add_u64 v[6:7], s[2:3], 0, v[22:23]
	v_cvt_pk_f16_f32 v3, v8, v9
	v_cvt_pk_f16_f32 v4, v4, v5
	v_cvt_pk_f16_f32 v5, v10, v11
	v_lshl_add_u64 v[6:7], v[6:7], 0, v[90:91]
	s_mov_b32 s17, 32
	v_mov_b32_e32 v145, v139
	v_mov_b32_e32 v147, v139
	v_mov_b32_e32 v149, v139
	v_mov_b32_e32 v151, v139
	global_store_dwordx4 v[6:7], v[2:5], off sc1
	s_mov_b32 s2, 0xe000
	v_mov_b32_e32 v6, v139
	v_mov_b32_e32 v2, v139
	v_mov_b32_e32 v3, v139
	v_mov_b32_e32 v4, v139
	v_mov_b32_e32 v5, v139
	v_mov_b32_e32 v7, v139
	v_mov_b32_e32 v8, v139
	v_mov_b32_e32 v9, v139
	v_mov_b32_e32 v10, v139
	v_mov_b32_e32 v11, v139
	v_mov_b32_e32 v12, v139
	v_mov_b32_e32 v13, v139
	v_mov_b32_e32 v14, v139
	v_mov_b32_e32 v15, v139
	v_mov_b32_e32 v16, v139
	v_mov_b32_e32 v17, v139
	v_mov_b32_e32 v18, v139
	v_mov_b32_e32 v19, v139
	v_mov_b32_e32 v20, v139
	v_mov_b32_e32 v21, v139
	v_mov_b32_e32 v22, v139
	v_mov_b32_e32 v24, v139
	v_mov_b32_e32 v25, v139
	v_mov_b32_e32 v26, v139
	v_mov_b32_e32 v27, v139
	v_mov_b32_e32 v28, v139
	v_mov_b32_e32 v29, v139
	v_mov_b32_e32 v30, v139
	v_mov_b32_e32 v31, v139
	v_mov_b32_e32 v32, v139
	v_mov_b32_e32 v33, v139
	v_mov_b32_e32 v34, v139
	v_mov_b32_e32 v35, v139
	v_mov_b32_e32 v36, v139
	v_mov_b32_e32 v37, v139
	v_mov_b32_e32 v38, v139
	v_mov_b32_e32 v39, v139
	v_mov_b32_e32 v40, v139
	v_mov_b32_e32 v41, v139
	v_mov_b32_e32 v42, v139
	v_mov_b32_e32 v43, v139
	v_mov_b32_e32 v44, v139
	v_mov_b32_e32 v45, v139
	v_mov_b32_e32 v46, v139
	v_mov_b32_e32 v48, v139
	v_mov_b32_e32 v49, v139
	v_mov_b32_e32 v50, v139
	v_mov_b32_e32 v51, v139
	v_mov_b32_e32 v52, v139
	v_mov_b32_e32 v53, v139
	v_mov_b32_e32 v54, v139
	v_mov_b32_e32 v55, v139
	v_mov_b32_e32 v56, v139
	v_mov_b32_e32 v57, v139
	v_mov_b32_e32 v58, v139
	v_mov_b32_e32 v59, v139
	v_mov_b32_e32 v60, v139
	v_mov_b32_e32 v61, v139
	v_mov_b32_e32 v62, v139
	v_mov_b32_e32 v63, v139
	v_mov_b32_e32 v64, v139
	v_mov_b32_e32 v65, v139
	v_mov_b32_e32 v66, v139
	v_mov_b32_e32 v67, v139
	v_mov_b32_e32 v68, v139
	v_mov_b32_e32 v69, v139
	v_mov_b32_e32 v70, v139
	v_mov_b32_e32 v72, v139
	v_mov_b32_e32 v73, v139
	v_mov_b32_e32 v74, v139
	v_mov_b32_e32 v75, v139
	v_mov_b32_e32 v76, v139
	v_mov_b32_e32 v77, v139
	v_mov_b32_e32 v78, v139
	v_mov_b32_e32 v79, v139
	v_mov_b32_e32 v80, v139
	v_mov_b32_e32 v81, v139
	v_mov_b32_e32 v82, v139
	v_mov_b32_e32 v83, v139
	v_mov_b32_e32 v84, v139
	v_mov_b32_e32 v86, v139
	v_mov_b32_e32 v87, v139
	v_mov_b32_e32 v88, v139
	v_mov_b32_e32 v89, v139
	v_mov_b32_e32 v90, v139
	v_mov_b32_e32 v92, v139
	v_mov_b32_e32 v93, v139
	v_mov_b32_e32 v94, v139
	v_mov_b32_e32 v95, v139
	v_mov_b32_e32 v96, v139

.LBB1_14:
	s_add_i32 s14, s16, s8
	s_cmpk_lt_i32 s14, 0x400
	s_waitcnt lgkmcnt(0)
	v_mov_b32_e32 v1, s7
	v_mov_b32_e32 v99, s6
	s_cselect_b64 vcc, -1, 0
	s_ashr_i32 s2, s14, 10
	v_cndmask_b32_e32 v98, v1, v99, vcc
	s_ashr_i32 s3, s2, 31
	v_pk_mul_f32 v[94:95], v[98:99], v[94:95] op_sel_hi:[0,1]
	v_pk_mul_f32 v[90:91], v[98:99], v[90:91] op_sel_hi:[0,1]
	s_bfe_u32 s12, s14, 0x40006
	s_lshl_b64 s[2:3], s[2:3], 24
	v_pk_mul_f32 v[100:101], v[98:99], v[92:93] op_sel_hi:[0,1]
	v_cvt_pk_f16_f32 v92, v94, v95
	v_cvt_pk_f16_f32 v94, v90, v91
	s_add_u32 s2, s4, s2
	v_or_b32_e32 v90, s12, v138
	v_mov_b32_e32 v91, v139
	v_pk_mul_f32 v[96:97], v[98:99], v[96:97] op_sel_hi:[0,1]
	s_addc_u32 s3, s5, s3
	v_lshlrev_b64 v[90:91], 18, v[90:91]
	v_cvt_pk_f16_f32 v93, v96, v97
	v_lshl_add_u64 v[90:91], s[2:3], 0, v[90:91]
	v_lshlrev_b64 v[96:97], 1, v[142:143]
	s_add_i32 s15, s14, 32
	v_cvt_pk_f16_f32 v95, v100, v101
	v_lshl_add_u64 v[100:101], v[90:91], 0, v[96:97]
	v_lshlrev_b64 v[90:91], 1, v[144:145]
	s_cmpk_lt_i32 s14, 0x3e0
	v_lshl_add_u64 v[100:101], v[100:101], 0, v[90:91]
	s_cselect_b64 vcc, -1, 0
	s_ashr_i32 s6, s15, 10
	global_store_dwordx4 v[100:101], v[92:95], off sc1
	s_ashr_i32 s7, s6, 31
	s_bfe_u32 s13, s15, 0x40006
	v_cndmask_b32_e32 v92, v1, v99, vcc
	v_pk_mul_f32 v[88:89], v[92:93], v[88:89] op_sel_hi:[0,1]
	v_pk_mul_f32 v[86:87], v[92:93], v[86:87] op_sel_hi:[0,1]
	v_pk_mul_f32 v[84:85], v[92:93], v[84:85] op_sel_hi:[0,1]
	s_lshl_b64 s[6:7], s[6:7], 24
	v_pk_mul_f32 v[82:83], v[92:93], v[82:83] op_sel_hi:[0,1]
	v_cvt_pk_f16_f32 v86, v86, v87
	v_cvt_pk_f16_f32 v87, v88, v89
	v_cvt_pk_f16_f32 v89, v84, v85
	s_add_u32 s6, s4, s6
	v_or_b32_e32 v84, s13, v138
	v_mov_b32_e32 v85, v139
	v_cvt_pk_f16_f32 v88, v82, v83
	v_and_or_b32 v82, s15, 32, v155
	s_addc_u32 s7, s5, s7
	v_lshlrev_b64 v[84:85], 18, v[84:85]
	s_add_i32 s15, s14, 64
	v_mov_b32_e32 v83, 0
	v_lshl_add_u64 v[84:85], s[6:7], 0, v[84:85]
	s_cmpk_lt_i32 s14, 0x3c0
	v_lshl_add_u64 v[94:95], v[84:85], 0, v[96:97]
	v_lshlrev_b64 v[84:85], 1, v[82:83]
	s_cselect_b64 vcc, -1, 0
	s_ashr_i32 s16, s15, 10
	v_lshl_add_u64 v[82:83], v[94:95], 0, v[84:85]
	s_ashr_i32 s17, s16, 31
	global_store_dwordx4 v[82:83], v[86:89], off sc1
	v_cndmask_b32_e32 v82, v1, v99, vcc
	s_bfe_u32 s14, s15, 0x40006
	s_lshl_b64 s[16:17], s[16:17], 24
	v_pk_mul_f32 v[78:79], v[82:83], v[78:79] op_sel_hi:[0,1]
	s_add_u32 s4, s4, s16
	v_or_b32_e32 v138, s14, v138
	v_pk_mul_f32 v[86:87], v[82:83], v[76:77] op_sel_hi:[0,1]
	v_pk_mul_f32 v[76:77], v[82:83], v[74:75] op_sel_hi:[0,1]
	v_cvt_pk_f16_f32 v74, v78, v79
	s_addc_u32 s5, s5, s17
	v_lshlrev_b64 v[78:79], 18, v[138:139]
	v_lshl_add_u64 v[78:79], s[4:5], 0, v[78:79]
	v_pk_mul_f32 v[80:81], v[82:83], v[80:81] op_sel_hi:[0,1]
	v_lshl_add_u64 v[78:79], v[78:79], 0, v[96:97]
	v_cvt_pk_f16_f32 v75, v80, v81
	v_cvt_pk_f16_f32 v76, v76, v77
	v_cvt_pk_f16_f32 v77, v86, v87
	v_lshl_add_u64 v[78:79], v[78:79], 0, v[90:91]
	v_pk_mul_f32 v[70:71], v[98:99], v[70:71] op_sel_hi:[0,1]
	global_store_dwordx4 v[78:79], v[74:77], off sc1
	v_pk_mul_f32 v[72:73], v[98:99], v[72:73] op_sel_hi:[0,1]
	v_pk_mul_f32 v[62:63], v[92:93], v[62:63] op_sel_hi:[0,1]
	v_pk_mul_f32 v[74:75], v[98:99], v[68:69] op_sel_hi:[0,1]
	v_pk_mul_f32 v[68:69], v[98:99], v[66:67] op_sel_hi:[0,1]
	v_cvt_pk_f16_f32 v66, v70, v71
	v_or_b32_e32 v70, s12, v140
	v_mov_b32_e32 v71, v141
	v_lshlrev_b64 v[70:71], 18, v[70:71]
	v_cvt_pk_f16_f32 v67, v72, v73
	v_lshl_add_u64 v[70:71], s[2:3], 0, v[70:71]
	v_lshlrev_b64 v[72:73], 1, v[146:147]
	v_lshl_add_u64 v[70:71], v[70:71], 0, v[72:73]
	v_cvt_pk_f16_f32 v68, v68, v69
	v_cvt_pk_f16_f32 v69, v74, v75
	v_lshl_add_u64 v[70:71], v[70:71], 0, v[90:91]
	global_store_dwordx4 v[70:71], v[66:69], off sc1
	v_pk_mul_f32 v[64:65], v[92:93], v[64:65] op_sel_hi:[0,1]
	v_pk_mul_f32 v[54:55], v[82:83], v[54:55] op_sel_hi:[0,1]
	v_pk_mul_f32 v[66:67], v[92:93], v[60:61] op_sel_hi:[0,1]
	v_pk_mul_f32 v[60:61], v[92:93], v[58:59] op_sel_hi:[0,1]
	v_cvt_pk_f16_f32 v58, v62, v63
	v_or_b32_e32 v62, s13, v140
	v_mov_b32_e32 v63, v141
	v_lshlrev_b64 v[62:63], 18, v[62:63]
	v_lshl_add_u64 v[62:63], s[6:7], 0, v[62:63]
	v_lshl_add_u64 v[62:63], v[62:63], 0, v[72:73]
	v_cvt_pk_f16_f32 v59, v64, v65
	v_cvt_pk_f16_f32 v60, v60, v61
	v_cvt_pk_f16_f32 v61, v66, v67
	v_lshl_add_u64 v[62:63], v[62:63], 0, v[84:85]
	global_store_dwordx4 v[62:63], v[58:61], off sc1
	v_pk_mul_f32 v[56:57], v[82:83], v[56:57] op_sel_hi:[0,1]
	v_pk_mul_f32 v[46:47], v[98:99], v[46:47] op_sel_hi:[0,1]
	v_pk_mul_f32 v[58:59], v[82:83], v[52:53] op_sel_hi:[0,1]
	v_pk_mul_f32 v[52:53], v[82:83], v[50:51] op_sel_hi:[0,1]
	v_cvt_pk_f16_f32 v50, v54, v55
	v_or_b32_e32 v54, s14, v140
	v_mov_b32_e32 v55, v141
	v_lshlrev_b64 v[54:55], 18, v[54:55]
	v_lshl_add_u64 v[54:55], s[4:5], 0, v[54:55]
	v_lshl_add_u64 v[54:55], v[54:55], 0, v[72:73]
	v_cvt_pk_f16_f32 v51, v56, v57
	v_cvt_pk_f16_f32 v52, v52, v53
	v_cvt_pk_f16_f32 v53, v58, v59
	v_lshl_add_u64 v[54:55], v[54:55], 0, v[90:91]
	global_store_dwordx4 v[54:55], v[50:53], off sc1
	v_pk_mul_f32 v[48:49], v[98:99], v[48:49] op_sel_hi:[0,1]
	v_pk_mul_f32 v[38:39], v[92:93], v[38:39] op_sel_hi:[0,1]
	v_pk_mul_f32 v[50:51], v[98:99], v[44:45] op_sel_hi:[0,1]
	v_pk_mul_f32 v[44:45], v[98:99], v[42:43] op_sel_hi:[0,1]
	v_cvt_pk_f16_f32 v42, v46, v47
	v_or_b32_e32 v46, s12, v140
	v_mov_b32_e32 v47, v141
	v_lshlrev_b64 v[46:47], 18, v[46:47]
	v_cvt_pk_f16_f32 v43, v48, v49
	v_lshl_add_u64 v[46:47], s[2:3], 0, v[46:47]
	v_lshlrev_b64 v[48:49], 1, v[148:149]
	v_lshl_add_u64 v[46:47], v[46:47], 0, v[48:49]
	v_cvt_pk_f16_f32 v44, v44, v45
	v_cvt_pk_f16_f32 v45, v50, v51
	v_lshl_add_u64 v[46:47], v[46:47], 0, v[90:91]
	global_store_dwordx4 v[46:47], v[42:45], off sc1
	v_pk_mul_f32 v[40:41], v[92:93], v[40:41] op_sel_hi:[0,1]
	v_pk_mul_f32 v[30:31], v[82:83], v[30:31] op_sel_hi:[0,1]
	v_pk_mul_f32 v[42:43], v[92:93], v[36:37] op_sel_hi:[0,1]
	v_pk_mul_f32 v[36:37], v[92:93], v[34:35] op_sel_hi:[0,1]
	v_cvt_pk_f16_f32 v34, v38, v39
	v_or_b32_e32 v38, s13, v140
	v_mov_b32_e32 v39, v141
	v_lshlrev_b64 v[38:39], 18, v[38:39]
	v_lshl_add_u64 v[38:39], s[6:7], 0, v[38:39]
	v_lshl_add_u64 v[38:39], v[38:39], 0, v[48:49]
	v_cvt_pk_f16_f32 v35, v40, v41
	v_cvt_pk_f16_f32 v36, v36, v37
	v_cvt_pk_f16_f32 v37, v42, v43
	v_lshl_add_u64 v[38:39], v[38:39], 0, v[84:85]
	global_store_dwordx4 v[38:39], v[34:37], off sc1
	v_pk_mul_f32 v[32:33], v[82:83], v[32:33] op_sel_hi:[0,1]
	v_pk_mul_f32 v[22:23], v[98:99], v[22:23] op_sel_hi:[0,1]
	v_pk_mul_f32 v[34:35], v[82:83], v[28:29] op_sel_hi:[0,1]
	v_pk_mul_f32 v[28:29], v[82:83], v[26:27] op_sel_hi:[0,1]
	v_cvt_pk_f16_f32 v26, v30, v31
	v_or_b32_e32 v30, s14, v140
	v_mov_b32_e32 v31, v141
	v_lshlrev_b64 v[30:31], 18, v[30:31]
	v_lshl_add_u64 v[30:31], s[4:5], 0, v[30:31]
	v_lshl_add_u64 v[30:31], v[30:31], 0, v[48:49]
	v_cvt_pk_f16_f32 v27, v32, v33
	v_cvt_pk_f16_f32 v28, v28, v29
	v_cvt_pk_f16_f32 v29, v34, v35
	v_lshl_add_u64 v[30:31], v[30:31], 0, v[90:91]
	global_store_dwordx4 v[30:31], v[26:29], off sc1
	v_pk_mul_f32 v[24:25], v[98:99], v[24:25] op_sel_hi:[0,1]
	v_pk_mul_f32 v[14:15], v[92:93], v[14:15] op_sel_hi:[0,1]
	v_pk_mul_f32 v[26:27], v[98:99], v[20:21] op_sel_hi:[0,1]
	v_pk_mul_f32 v[20:21], v[98:99], v[18:19] op_sel_hi:[0,1]
	v_cvt_pk_f16_f32 v18, v22, v23
	v_or_b32_e32 v22, s12, v140
	v_mov_b32_e32 v23, v141
	v_lshlrev_b64 v[22:23], 18, v[22:23]
	v_cvt_pk_f16_f32 v19, v24, v25
	v_lshl_add_u64 v[22:23], s[2:3], 0, v[22:23]
	v_lshlrev_b64 v[24:25], 1, v[150:151]
	v_lshl_add_u64 v[22:23], v[22:23], 0, v[24:25]
	v_cvt_pk_f16_f32 v20, v20, v21
	v_cvt_pk_f16_f32 v21, v26, v27
	v_lshl_add_u64 v[22:23], v[22:23], 0, v[90:91]
	global_store_dwordx4 v[22:23], v[18:21], off sc1
	v_pk_mul_f32 v[16:17], v[92:93], v[16:17] op_sel_hi:[0,1]
	v_pk_mul_f32 v[6:7], v[82:83], v[6:7] op_sel_hi:[0,1]
	v_pk_mul_f32 v[18:19], v[92:93], v[12:13] op_sel_hi:[0,1]
	v_pk_mul_f32 v[12:13], v[92:93], v[10:11] op_sel_hi:[0,1]
	v_cvt_pk_f16_f32 v10, v14, v15
	v_or_b32_e32 v14, s13, v140
	v_mov_b32_e32 v15, v141
	v_lshlrev_b64 v[14:15], 18, v[14:15]
	v_lshl_add_u64 v[14:15], s[6:7], 0, v[14:15]
	v_lshl_add_u64 v[14:15], v[14:15], 0, v[24:25]
	v_cvt_pk_f16_f32 v11, v16, v17
	v_cvt_pk_f16_f32 v12, v12, v13
	v_cvt_pk_f16_f32 v13, v18, v19
	v_lshl_add_u64 v[14:15], v[14:15], 0, v[84:85]
	v_or_b32_e32 v140, s14, v140
	global_store_dwordx4 v[14:15], v[10:13], off sc1
	v_pk_mul_f32 v[8:9], v[82:83], v[8:9] op_sel_hi:[0,1]
	s_nop 0
	v_pk_mul_f32 v[10:11], v[82:83], v[4:5] op_sel_hi:[0,1]
	v_pk_mul_f32 v[4:5], v[82:83], v[2:3] op_sel_hi:[0,1]
	v_cvt_pk_f16_f32 v2, v6, v7
	v_lshlrev_b64 v[6:7], 18, v[140:141]
	v_lshl_add_u64 v[6:7], s[4:5], 0, v[6:7]
	v_lshl_add_u64 v[6:7], v[6:7], 0, v[24:25]
	v_cvt_pk_f16_f32 v3, v8, v9
	v_cvt_pk_f16_f32 v4, v4, v5
	v_cvt_pk_f16_f32 v5, v10, v11
	v_lshl_add_u64 v[6:7], v[6:7], 0, v[90:91]
	global_store_dwordx4 v[6:7], v[2:5], off sc1
	s_branch .LBB1_2

.LBB2_30:
	v_add_f32_e32 v50, v66, v67
	v_add_f32_e32 v50, v68, v50
	v_add_f32_e32 v50, v69, v50
	v_add_f32_e32 v50, v70, v50
	v_add_f32_e32 v50, v71, v50
	v_add_f32_e32 v50, v72, v50
	v_add_f32_e32 v50, v73, v50
	v_add_f32_e32 v50, v74, v50
	v_add_f32_e32 v50, v75, v50
	v_add_f32_e32 v50, v76, v50
	v_add_f32_e32 v50, v77, v50
	v_add_f32_e32 v50, v78, v50
	v_add_f32_e32 v50, v79, v50
	v_add_f32_e32 v50, v80, v50
	v_add_f32_e32 v50, v81, v50
	v_add_f32_e32 v50, v34, v50
	v_add_f32_e32 v50, v35, v50
	v_add_f32_e32 v50, v36, v50
	v_add_f32_e32 v50, v37, v50
	v_add_f32_e32 v50, v38, v50
	v_add_f32_e32 v50, v39, v50
	v_add_f32_e32 v50, v40, v50
	v_add_f32_e32 v50, v41, v50
	v_add_f32_e32 v50, v42, v50
	v_add_f32_e32 v50, v43, v50
	v_add_f32_e32 v50, v44, v50
	v_add_f32_e32 v50, v45, v50
	v_add_f32_e32 v50, v46, v50
	v_add_f32_e32 v50, v47, v50
	v_add_f32_e32 v50, v48, v50
	v_add_f32_e32 v50, v49, v50
	v_add_f32_e32 v50, v86, v50
	v_cvt_pk_f16_f32 v34, v34, v35
	v_cvt_pk_f16_f32 v52, v66, v67
	v_cvt_pk_f16_f32 v53, v68, v69
	v_cvt_pk_f16_f32 v54, v70, v71
	v_cvt_pk_f16_f32 v55, v72, v73
	v_cvt_pk_f16_f32 v56, v74, v75
	v_cvt_pk_f16_f32 v57, v76, v77
	v_cvt_pk_f16_f32 v58, v78, v79
	v_cvt_pk_f16_f32 v59, v80, v81
	v_cvt_pk_f16_f32 v35, v36, v37
	v_cvt_pk_f16_f32 v36, v38, v39
	v_cvt_pk_f16_f32 v37, v40, v41
	v_cvt_pk_f16_f32 v38, v42, v43
	v_cvt_pk_f16_f32 v39, v44, v45
	v_cvt_pk_f16_f32 v40, v46, v47
	v_cvt_pk_f16_f32 v41, v48, v49
	v_or_b32_e32 v42, 0x8000, v203
	v_add_u32_e32 v199, v42, v200
	v_add_u32_e32 v197, v42, v202
	ds_read_b64_tr_b16 v[42:43],v199 offset:0
	ds_read_b64_tr_b16 v[44:45],v199 offset:1024
	ds_read_b64_tr_b16 v[46:47],v199 offset:2048
	ds_read_b64_tr_b16 v[48:49],v199 offset:3072
	ds_read_b64_tr_b16 v[60:61],v199 offset:4096
	ds_read_b64_tr_b16 v[62:63],v199 offset:5120
	ds_read_b64_tr_b16 v[64:65],v199 offset:6144
	ds_read_b64_tr_b16 v[66:67],v199 offset:7168
	s_waitcnt lgkmcnt(0)
	s_nop 0
	v_mfma_f32_32x32x16_f16 v[2:17], v[52:55], v[42:45], v[2:17]
	ds_read_b64_tr_b16 v[42:43],v197 offset:0
	ds_read_b64_tr_b16 v[44:45],v197 offset:1024
	v_mfma_f32_32x32x16_f16 v[2:17], v[56:59], v[46:49], v[2:17]
	ds_read_b64_tr_b16 v[46:47],v197 offset:2048
	ds_read_b64_tr_b16 v[48:49],v197 offset:3072
	v_mfma_f32_32x32x16_f16 v[2:17], v[34:37], v[60:63], v[2:17]
	ds_read_b64_tr_b16 v[60:61],v197 offset:4096
	ds_read_b64_tr_b16 v[62:63],v197 offset:5120
	ds_read_b64_tr_b16 v[68:69],v197 offset:6144
	ds_read_b64_tr_b16 v[70:71],v197 offset:7168
	s_waitcnt lgkmcnt(0)
	v_mfma_f32_32x32x16_f16 v[2:17], v[38:41], v[64:67], v[2:17]
	v_mfma_f32_32x32x16_f16 v[18:33], v[52:55], v[42:45], v[18:33]
	v_mfma_f32_32x32x16_f16 v[18:33], v[56:59], v[46:49], v[18:33]
	v_mfma_f32_32x32x16_f16 v[18:33], v[34:37], v[60:63], v[18:33]
	v_mov_b32_e32 v34, v50
	s_nop 1
	v_permlane32_swap_b32_e32 v50, v34
	v_mfma_f32_32x32x16_f16 v[18:33], v[38:41], v[68:71], v[18:33]
	s_and_saveexec_b64 s[2:3], s[0:1]
	v_add_f32_e32 v34, v50, v34
	ds_write_b32 v204, v34 offset:49280
	s_or_b64 exec, exec, s[2:3]
	s_waitcnt lgkmcnt(0)
	ds_read_b128 v[34:37], v213 offset:49280
	ds_read_b128 v[38:41], v213 offset:49312
	s_lshl_b32 s20, s33, 12
	v_or_b32_e32 v50, s20, v201
	v_lshl_add_u32 v50, v191, 1, v50
	s_waitcnt lgkmcnt(1)
	v_rcp_f32_e32 v42, v34
	v_rcp_f32_e32 v43, v35
	v_rcp_f32_e32 v44, v36
	v_rcp_f32_e32 v45, v37
	v_fma_mixlo_f16 v2, v2, v42, 0
	ds_write_b16 v50, v2 offset:51200
	v_fma_mixlo_f16 v2, v18, v42, 0
	ds_write_b16 v50, v2 offset:51264
	v_fma_mixlo_f16 v2, v3, v43, 0
	ds_write_b16 v50, v2 offset:51328
	v_fma_mixlo_f16 v2, v19, v43, 0
	s_waitcnt lgkmcnt(3)
	v_rcp_f32_e32 v46, v38
	ds_write_b16 v50, v2 offset:51392
	v_fma_mixlo_f16 v2, v4, v44, 0
	ds_write_b16 v50, v2 offset:51456
	v_fma_mixlo_f16 v2, v20, v44, 0
	v_rcp_f32_e32 v47, v39
	ds_write_b16 v50, v2 offset:51520
	v_fma_mixlo_f16 v2, v5, v45, 0
	ds_read_b128 v[34:37], v213 offset:49344
	ds_write_b16 v50, v2 offset:51584
	v_fma_mixlo_f16 v2, v21, v45, 0
	v_rcp_f32_e32 v48, v40
	ds_write_b16 v50, v2 offset:51648
	v_fma_mixlo_f16 v2, v6, v46, 0
	ds_write_b16 v50, v2 offset:52224
	v_fma_mixlo_f16 v2, v22, v46, 0
	v_rcp_f32_e32 v49, v41
	ds_write_b16 v50, v2 offset:52288
	v_fma_mixlo_f16 v2, v7, v47, 0
	ds_write_b16 v50, v2 offset:52352
	v_fma_mixlo_f16 v2, v23, v47, 0
	ds_read_b128 v[38:41], v213 offset:49376
	s_waitcnt lgkmcnt(6)
	v_rcp_f32_e32 v34, v34
	ds_write_b16 v50, v2 offset:52416
	v_fma_mixlo_f16 v2, v8, v48, 0
	ds_write_b16 v50, v2 offset:52480
	v_fma_mixlo_f16 v2, v24, v48, 0
	v_rcp_f32_e32 v35, v35
	ds_write_b16 v50, v2 offset:52544
	v_fma_mixlo_f16 v2, v9, v49, 0
	ds_write_b16 v50, v2 offset:52608
	v_fma_mixlo_f16 v2, v25, v49, 0
	v_rcp_f32_e32 v36, v36
	ds_write_b16 v50, v2 offset:52672
	v_fma_mixlo_f16 v2, v10, v34, 0
	ds_write_b16 v50, v2 offset:53248
	v_fma_mixlo_f16 v2, v26, v34, 0
	v_rcp_f32_e32 v37, v37
	ds_write_b16 v50, v2 offset:53312
	v_fma_mixlo_f16 v2, v11, v35, 0
	ds_write_b16 v50, v2 offset:53376
	v_fma_mixlo_f16 v2, v27, v35, 0
	s_waitcnt lgkmcnt(8)
	v_rcp_f32_e32 v38, v38
	ds_write_b16 v50, v2 offset:53440
	v_fma_mixlo_f16 v2, v12, v36, 0
	ds_write_b16 v50, v2 offset:53504
	v_fma_mixlo_f16 v2, v28, v36, 0
	v_rcp_f32_e32 v39, v39
	ds_write_b16 v50, v2 offset:53568
	v_fma_mixlo_f16 v2, v13, v37, 0
	ds_write_b16 v50, v2 offset:53632
	v_fma_mixlo_f16 v2, v29, v37, 0
	v_rcp_f32_e32 v40, v40
	ds_write_b16 v50, v2 offset:53696
	v_fma_mixlo_f16 v2, v14, v38, 0
	ds_write_b16 v50, v2 offset:54272
	v_fma_mixlo_f16 v2, v30, v38, 0
	v_rcp_f32_e32 v41, v41
	ds_write_b16 v50, v2 offset:54336
	v_fma_mixlo_f16 v2, v15, v39, 0
	ds_write_b16 v50, v2 offset:54400
	v_fma_mixlo_f16 v2, v31, v39, 0
	ds_write_b16 v50, v2 offset:54464
	v_fma_mixlo_f16 v2, v16, v40, 0
	ds_write_b16 v50, v2 offset:54528
	v_fma_mixlo_f16 v2, v32, v40, 0
	ds_write_b16 v50, v2 offset:54592
	v_fma_mixlo_f16 v2, v17, v41, 0
	s_lshl_b64 s[2:3], s[18:19], 11
	ds_write_b16 v50, v2 offset:54656
	v_fma_mixlo_f16 v2, v33, v41, 0
	ds_write_b16 v50, v2 offset:54720
	s_or_b64 s[18:19], s[2:3], s[12:13]
	v_lshlrev_b32_e32 v2, 11, v0
	v_lshlrev_b32_e32 v213, 4, v1
	v_and_b32_e32 v2, 0x2000, v2
	v_mov_b32_e32 v195, 0
	s_add_u32 s18, s31, s18
	v_or_b32_e32 v14, s20, v213
	v_lshl_or_b32 v194, s30, 14, v2
	s_addc_u32 s19, 0, s19
	v_lshlrev_b32_e32 v2, 1, v193
	v_mov_b32_e32 v3, v195
	v_lshlrev_b32_e32 v214, 7, v190
	s_waitcnt lgkmcnt(0)
	v_lshl_add_u64 v[10:11], s[18:19], 0, v[194:195]
	v_lshl_add_u64 v[188:189], s[6:7], 0, v[2:3]
	v_or_b32_e32 v2, v14, v214
	ds_read_b128 v[2:5], v2 offset:51200
	v_or_b32_e32 v6, v10, v190
	v_mov_b32_e32 v7, v11
	v_or_b32_e32 v196, 8, v190
	v_lshlrev_b64 v[6:7], 6, v[6:7]
	v_lshlrev_b32_e32 v215, 7, v196
	v_lshl_add_u64 v[12:13], v[188:189], 0, v[6:7]
	v_or_b32_e32 v6, v14, v215
	ds_read_b128 v[6:9], v6 offset:51200
	s_waitcnt lgkmcnt(1)
	global_store_dwordx4 v[12:13], v[2:5], off sc1
	v_or_b32_e32 v198, 16, v190
	v_lshlrev_b32_e32 v216, 7, v198
	v_or_b32_e32 v2, v10, v196
	v_mov_b32_e32 v3, v11
	v_lshlrev_b64 v[2:3], 6, v[2:3]
	v_lshl_add_u64 v[2:3], v[188:189], 0, v[2:3]
	s_waitcnt lgkmcnt(0)
	global_store_dwordx4 v[2:3], v[6:9], off sc1
	v_or_b32_e32 v2, v14, v216
	v_or_b32_e32 v200, 24, v190
	v_or_b32_e32 v6, v10, v198
	v_mov_b32_e32 v7, v11
	ds_read_b128 v[2:5], v2 offset:51200
	v_lshlrev_b64 v[6:7], 6, v[6:7]
	v_lshlrev_b32_e32 v217, 7, v200
	v_lshl_add_u64 v[12:13], v[188:189], 0, v[6:7]
	v_or_b32_e32 v6, v14, v217
	ds_read_b128 v[6:9], v6 offset:51200
	v_or_b32_e32 v10, v10, v200
	s_waitcnt lgkmcnt(1)
	global_store_dwordx4 v[12:13], v[2:5], off sc1
	v_readfirstlane_b32 s20, v0
	s_lshr_b32 s19, s20, 6
	v_lshlrev_b64 v[2:3], 6, v[10:11]
	v_lshl_add_u64 v[2:3], v[188:189], 0, v[2:3]
	s_waitcnt lgkmcnt(0)
	global_store_dwordx4 v[2:3], v[6:9], off sc1
	v_lshl_or_b32 v2, s19, 3, v190
	s_xor_b32 s6, s12, 0x700
	v_mov_b32_e32 v3, v195
	v_lshrrev_b32_e32 v88, 1, v2
	s_or_b32 s7, s8, s6
	s_lshl_b32 s18, s19, 5
	v_lshlrev_b64 v[84:85], 7, v[2:3]
	v_xor_b32_e32 v2, v88, v0
	s_add_u32 s8, s7, s18
	v_lshlrev_b32_e32 v2, 4, v2
	s_addc_u32 s9, s9, 0
	v_lshl_add_u64 v[4:5], s[14:15], 0, v[84:85]
	v_and_b32_e32 v2, 0x70, v2
	s_lshl_b64 s[8:9], s[8:9], 7
	v_lshl_add_u64 v[184:185], v[4:5], 0, v[2:3]
	v_lshlrev_b32_e32 v4, 1, v190
	s_waitcnt lgkmcnt(0)
	s_barrier
	s_add_u32 s12, s4, s8
	v_bitop3_b32 v1, v4, v1, 4 bitop3:0x6c
	s_addc_u32 s13, s5, s9
	v_lshl_add_u64 v[2:3], s[10:11], 0, v[84:85]
	v_lshlrev_b32_e32 v86, 4, v1
	v_mov_b32_e32 v87, v195
	s_lshl_b32 s22, s19, 10
	s_mov_b32 s7, m0
	s_mov_b32 m0, s22
	s_nop 0
	global_load_lds_dwordx4 v[184:185], off
	s_mov_b32 m0, s7
	v_lshl_add_u64 v[202:203], v[2:3], 0, v[86:87]
	s_add_i32 s21, s22, 0x6000
	s_mov_b32 s7, m0
	s_mov_b32 m0, s21
	s_nop 0
	global_load_lds_dwordx4 v[202:203], off
	s_mov_b32 m0, s7
	s_mov_b64 s[8:9], 0x2000
	v_lshl_add_u64 v[2:3], v[184:185], 0, s[8:9]
	s_add_i32 s23, s22, 0x2000
	s_mov_b32 s7, m0
	s_mov_b32 m0, s23
	s_nop 0
	global_load_lds_dwordx4 v[2:3], off
	s_mov_b32 m0, s7
	v_lshlrev_b32_e32 v1, 1, v192
	global_load_dwordx4 v[156:159], v1, s[12:13]
	global_load_dwordx4 v[148:151], v1, s[12:13] offset:32
	global_load_dwordx4 v[140:143], v1, s[12:13] offset:64
	global_load_dwordx4 v[132:135], v1, s[12:13] offset:96
	v_mov_b32_e32 v2, v195
	v_mov_b32_e32 v3, v195
	v_mov_b32_e32 v4, v195
	v_mov_b32_e32 v5, v195
	v_mov_b32_e32 v6, v195
	v_mov_b32_e32 v7, v195
	v_mov_b32_e32 v8, v195
	v_mov_b32_e32 v9, v195
	v_mov_b32_e32 v10, v195
	v_mov_b32_e32 v11, v195
	v_mov_b32_e32 v12, v195
	v_mov_b32_e32 v13, v195
	v_mov_b32_e32 v14, v195
	v_mov_b32_e32 v15, v195
	v_mov_b32_e32 v16, v195
	v_mov_b32_e32 v17, v195
	s_mov_b64 s[10:11], 0x4000
	v_lshl_add_u64 v[18:19], v[184:185], 0, s[10:11]
	s_add_i32 s7, s22, 0x4000
	s_mov_b32 s12, m0
	s_mov_b32 m0, s7
	s_nop 0
	global_load_lds_dwordx4 v[18:19], off
	s_mov_b32 m0, s12
	s_waitcnt vmcnt(3) lgkmcnt(0)
	s_barrier
	ds_read_b128 v[34:37], v211
	s_waitcnt vmcnt(3) lgkmcnt(0)
	v_mfma_f32_32x32x16_f16 v[18:33], v[34:37], v[156:159], v[2:17]
	ds_read_b128 v[34:37], v211 offset:4096
	s_and_b32 s12, s20, 0x3fffffc0
	s_lshl_b32 s24, s12, 2
	s_mov_b64 s[12:13], 0x6000
	s_add_i32 s20, s22, 0x8000
	v_bitop3_b32 v0, v88, 7, v0 bitop3:0x48
	v_lshlrev_b32_e32 v0, 4, v0
	s_waitcnt lgkmcnt(0)
	v_mfma_f32_32x32x16_f16 v[2:17], v[34:37], v[156:159], v[2:17]
	ds_read_b128 v[34:37], v210
	s_mov_b32 s7, 0
	s_movk_i32 s28, 0x2000
	s_movk_i32 s25, 0x4000
	v_lshl_or_b32 v218, v191, 2, s24
	s_mov_b32 s26, -1
	s_mov_b32 s27, 0x41000000
	s_waitcnt vmcnt(2) lgkmcnt(0)
	v_mfma_f32_32x32x16_f16 v[18:33], v[34:37], v[148:151], v[18:33]
	ds_read_b128 v[34:37], v210 offset:4096
	v_mov_b32_e32 v180, v195
	s_waitcnt lgkmcnt(0)
	v_mfma_f32_32x32x16_f16 v[2:17], v[34:37], v[148:151], v[2:17]
	ds_read_b128 v[34:37], v209
	s_waitcnt vmcnt(1) lgkmcnt(0)
	v_mfma_f32_32x32x16_f16 v[18:33], v[34:37], v[140:143], v[18:33]
	ds_read_b128 v[34:37], v209 offset:4096
	s_waitcnt lgkmcnt(0)
	v_mfma_f32_32x32x16_f16 v[2:17], v[34:37], v[140:143], v[2:17]
	ds_read_b128 v[34:37], v208
	s_waitcnt vmcnt(0) lgkmcnt(0)
	v_mfma_f32_32x32x16_f16 v[18:33], v[34:37], v[132:135], v[18:33]
	ds_read_b128 v[34:37], v208 offset:4096
	s_waitcnt lgkmcnt(0)
	v_mfma_f32_32x32x16_f16 v[2:17], v[34:37], v[132:135], v[2:17]
	s_nop 15
	s_nop 7
	s_nop 0
	v_max3_f32 v1, v18, v19, v2
	v_max3_f32 v34, v20, v21, v3
	s_nop 0
	v_max3_f32 v1, v1, v4, v5
	v_max3_f32 v34, v34, v24, v25
	s_nop 0
	v_max3_f32 v1, v1, v22, v23
	v_max3_f32 v34, v34, v8, v9
	s_nop 0
	v_max3_f32 v1, v1, v6, v7
	v_max3_f32 v34, v34, v28, v29
	s_nop 0
	v_max3_f32 v1, v1, v26, v27
	v_max3_f32 v34, v34, v12, v13
	s_nop 0
	v_max3_f32 v1, v1, v10, v11
	v_max3_f32 v34, v34, v32, v33
	s_nop 0
	v_max3_f32 v1, v1, v30, v31
	v_max3_f32 v34, v34, v16, v17
	s_nop 0
	v_max3_f32 v1, v1, v14, v15
	s_nop 0
	v_max_f32_e32 v1, v1, v34
	s_nop 0
	v_mov_b32_e32 v34, v1
	s_nop 1
	v_permlane32_swap_b32_e32 v1, v34
	v_max_f32_e32 v1, v1, v34
	s_nop 0
	v_add_f32_e32 v219, v195, v1
	v_sub_f32_e32 v48, v32, v1
	v_sub_f32_e32 v49, v33, v1
	v_sub_f32_e32 v2, v2, v1
	v_sub_f32_e32 v3, v3, v1
	v_sub_f32_e32 v18, v18, v1
	s_nop 0
	v_xor_b32_e32 v32, 0x80000000, v219
	v_mov_b32_e32 v33, v32
	v_mov_b32_e32 v34, v32
	v_mov_b32_e32 v35, v32
	v_mov_b32_e32 v36, v32
	v_mov_b32_e32 v37, v32
	v_mov_b32_e32 v38, v32
	v_mov_b32_e32 v39, v32
	v_mov_b32_e32 v40, v32
	v_mov_b32_e32 v41, v32
	v_mov_b32_e32 v42, v32
	v_mov_b32_e32 v43, v32
	v_mov_b32_e32 v44, v32
	v_mov_b32_e32 v45, v32
	v_mov_b32_e32 v46, v32
	v_mov_b32_e32 v47, v32
	s_waitcnt vmcnt(0) lgkmcnt(0)
	s_barrier
	v_exp_f32_e32 v78, v48
	v_exp_f32_e32 v79, v49
	v_exp_f32_e32 v48, v2
	v_exp_f32_e32 v49, v3
	v_lshl_add_u64 v[2:3], v[184:185], 0, s[12:13]
	s_mov_b32 s14, m0
	s_mov_b32 m0, s22
	s_nop 0
	global_load_lds_dwordx4 v[2:3], off
	s_mov_b32 m0, s14
	v_lshl_add_u64 v[2:3], v[202:203], 0, s[8:9]
	s_mov_b32 s14, m0
	s_mov_b32 m0, s20
	s_nop 0
	global_load_lds_dwordx4 v[2:3], off
	s_mov_b32 m0, s14
	ds_read_b128 v[80:83], v211 offset:8192
	ds_read_b128 v[168:171], v211 offset:12288
	ds_read_b128 v[164:167], v210 offset:8192
	ds_read_b128 v[160:163], v210 offset:12288
	ds_read_b128 v[124:127], v209 offset:8192
	ds_read_b128 v[120:123], v209 offset:12288
	ds_read_b128 v[116:119], v208 offset:8192
	ds_read_b128 v[112:115], v208 offset:12288
	v_sub_f32_e32 v19, v19, v1
	v_sub_f32_e32 v20, v20, v1
	v_sub_f32_e32 v4, v4, v1
	v_sub_f32_e32 v21, v21, v1
	v_sub_f32_e32 v5, v5, v1
	v_sub_f32_e32 v22, v22, v1
	v_sub_f32_e32 v6, v6, v1
	v_sub_f32_e32 v23, v23, v1
	v_sub_f32_e32 v7, v7, v1
	v_sub_f32_e32 v24, v24, v1
	v_sub_f32_e32 v8, v8, v1
	v_sub_f32_e32 v25, v25, v1
	v_sub_f32_e32 v9, v9, v1
	v_sub_f32_e32 v26, v26, v1
	v_sub_f32_e32 v10, v10, v1
	v_sub_f32_e32 v27, v27, v1
	v_sub_f32_e32 v11, v11, v1
	v_sub_f32_e32 v28, v28, v1
	v_sub_f32_e32 v12, v12, v1
	v_sub_f32_e32 v29, v29, v1
	v_sub_f32_e32 v13, v13, v1
	v_sub_f32_e32 v30, v30, v1
	v_sub_f32_e32 v14, v14, v1
	v_sub_f32_e32 v31, v31, v1
	v_sub_f32_e32 v15, v15, v1
	v_sub_f32_e32 v16, v16, v1
	v_sub_f32_e32 v1, v17, v1
	v_lshl_add_u64 v[2:3], s[16:17], 0, v[84:85]
	v_exp_f32_e32 v63, v1
	v_mov_b32_e32 v1, v195
	v_lshl_add_u64 v[0:1], v[2:3], 0, v[0:1]
	v_exp_f32_e32 v64, v18
	v_exp_f32_e32 v65, v19
	v_exp_f32_e32 v66, v20
	v_exp_f32_e32 v67, v21
	v_exp_f32_e32 v68, v22
	v_exp_f32_e32 v69, v23
	v_exp_f32_e32 v70, v24
	v_exp_f32_e32 v71, v25
	v_exp_f32_e32 v72, v26
	v_exp_f32_e32 v73, v27
	v_exp_f32_e32 v74, v28
	v_exp_f32_e32 v75, v29
	v_exp_f32_e32 v76, v30
	v_exp_f32_e32 v77, v31
	v_exp_f32_e32 v50, v4
	v_exp_f32_e32 v51, v5
	v_exp_f32_e32 v52, v6
	v_exp_f32_e32 v53, v7
	v_exp_f32_e32 v54, v8
	v_exp_f32_e32 v55, v9
	v_exp_f32_e32 v56, v10
	v_exp_f32_e32 v57, v11
	v_exp_f32_e32 v58, v12
	v_exp_f32_e32 v59, v13
	v_exp_f32_e32 v60, v14
	v_exp_f32_e32 v61, v15
	v_exp_f32_e32 v62, v16
	v_lshl_add_u64 v[0:1], s[4:5], 0, v[0:1]
	s_mov_b64 s[14:15], 0x1002000
	s_waitcnt vmcnt(2) lgkmcnt(0)
	s_barrier
	v_lshl_add_u64 v[186:187], v[0:1], 0, s[14:15]
	v_lshl_add_u64 v[0:1], v[2:3], 0, v[86:87]
	v_lshl_add_u64 v[0:1], s[4:5], 0, v[0:1]
	s_mov_b64 s[4:5], 0x2002000
	v_lshl_add_u64 v[192:193], v[0:1], 0, s[4:5]
	s_mov_b64 s[4:5], 0x8000
	s_mov_b32 s14, s7
	v_mov_b32_e32 v0, v195
	v_mov_b32_e32 v1, v195
	v_mov_b32_e32 v2, v195
	v_mov_b32_e32 v3, v195
	v_mov_b32_e32 v4, v195
	v_mov_b32_e32 v5, v195
	v_mov_b32_e32 v6, v195
	v_mov_b32_e32 v7, v195
	v_mov_b32_e32 v8, v195
	v_mov_b32_e32 v9, v195
	v_mov_b32_e32 v10, v195
	v_mov_b32_e32 v11, v195
	v_mov_b32_e32 v12, v195
	v_mov_b32_e32 v13, v195
	v_mov_b32_e32 v14, v195
	v_mov_b32_e32 v15, v195
	v_mov_b32_e32 v16, v195
	v_mov_b32_e32 v17, v195
	v_mov_b32_e32 v18, v195
	v_mov_b32_e32 v19, v195
	v_mov_b32_e32 v20, v195
	v_mov_b32_e32 v21, v195
	v_mov_b32_e32 v22, v195
	v_mov_b32_e32 v23, v195
	v_mov_b32_e32 v24, v195
	v_mov_b32_e32 v25, v195
	v_mov_b32_e32 v26, v195
	v_mov_b32_e32 v27, v195
	v_mov_b32_e32 v28, v195
	v_mov_b32_e32 v29, v195
	v_mov_b32_e32 v30, v195
	v_mov_b32_e32 v31, v195

.LBB2_62:
	v_add_f32_e32 v48, v64, v65
	v_add_f32_e32 v48, v66, v48
	v_add_f32_e32 v48, v67, v48
	v_add_f32_e32 v48, v68, v48
	v_add_f32_e32 v48, v69, v48
	v_add_f32_e32 v48, v70, v48
	v_add_f32_e32 v48, v71, v48
	v_add_f32_e32 v48, v72, v48
	v_add_f32_e32 v48, v73, v48
	v_add_f32_e32 v48, v74, v48
	v_add_f32_e32 v48, v75, v48
	v_add_f32_e32 v48, v76, v48
	v_add_f32_e32 v48, v77, v48
	v_add_f32_e32 v48, v78, v48
	v_add_f32_e32 v48, v79, v48
	v_add_f32_e32 v48, v32, v48
	v_add_f32_e32 v48, v33, v48
	v_add_f32_e32 v48, v34, v48
	v_add_f32_e32 v48, v35, v48
	v_add_f32_e32 v48, v36, v48
	v_add_f32_e32 v48, v37, v48
	v_add_f32_e32 v48, v38, v48
	v_add_f32_e32 v48, v39, v48
	v_add_f32_e32 v48, v40, v48
	v_add_f32_e32 v48, v41, v48
	v_add_f32_e32 v48, v42, v48
	v_add_f32_e32 v48, v43, v48
	v_add_f32_e32 v48, v44, v48
	v_add_f32_e32 v48, v45, v48
	v_add_f32_e32 v48, v46, v48
	v_add_f32_e32 v48, v47, v48
	v_add_f32_e32 v48, v84, v48
	v_cvt_pk_f16_f32 v32, v32, v33
	v_cvt_pk_f16_f32 v50, v64, v65
	v_cvt_pk_f16_f32 v51, v66, v67
	v_cvt_pk_f16_f32 v52, v68, v69
	v_cvt_pk_f16_f32 v53, v70, v71
	v_cvt_pk_f16_f32 v54, v72, v73
	v_cvt_pk_f16_f32 v55, v74, v75
	v_cvt_pk_f16_f32 v56, v76, v77
	v_cvt_pk_f16_f32 v57, v78, v79
	v_cvt_pk_f16_f32 v33, v34, v35
	v_cvt_pk_f16_f32 v34, v36, v37
	v_cvt_pk_f16_f32 v35, v38, v39
	v_cvt_pk_f16_f32 v36, v40, v41
	v_cvt_pk_f16_f32 v37, v42, v43
	v_cvt_pk_f16_f32 v38, v44, v45
	v_cvt_pk_f16_f32 v39, v46, v47
	ds_read_b64_tr_b16 v[40:41],v199 offset:0
	ds_read_b64_tr_b16 v[42:43],v199 offset:1024
	ds_read_b64_tr_b16 v[44:45],v199 offset:2048
	ds_read_b64_tr_b16 v[46:47],v199 offset:3072
	ds_read_b64_tr_b16 v[58:59],v199 offset:4096
	ds_read_b64_tr_b16 v[60:61],v199 offset:5120
	ds_read_b64_tr_b16 v[62:63],v199 offset:6144
	ds_read_b64_tr_b16 v[64:65],v199 offset:7168
	s_waitcnt lgkmcnt(0)
	s_nop 0
	v_mfma_f32_32x32x16_f16 v[0:15], v[50:53], v[40:43], v[0:15]
	ds_read_b64_tr_b16 v[40:41],v197 offset:0
	ds_read_b64_tr_b16 v[42:43],v197 offset:1024
	v_mfma_f32_32x32x16_f16 v[0:15], v[54:57], v[44:47], v[0:15]
	ds_read_b64_tr_b16 v[44:45],v197 offset:2048
	ds_read_b64_tr_b16 v[46:47],v197 offset:3072
	v_mfma_f32_32x32x16_f16 v[0:15], v[32:35], v[58:61], v[0:15]
	ds_read_b64_tr_b16 v[58:59],v197 offset:4096
	ds_read_b64_tr_b16 v[60:61],v197 offset:5120
	ds_read_b64_tr_b16 v[66:67],v197 offset:6144
	ds_read_b64_tr_b16 v[68:69],v197 offset:7168
	s_waitcnt lgkmcnt(0)
	v_mfma_f32_32x32x16_f16 v[0:15], v[36:39], v[62:65], v[0:15]
	v_mfma_f32_32x32x16_f16 v[16:31], v[50:53], v[40:43], v[16:31]
	v_mfma_f32_32x32x16_f16 v[16:31], v[54:57], v[44:47], v[16:31]
	v_mfma_f32_32x32x16_f16 v[16:31], v[32:35], v[58:61], v[16:31]
	v_mov_b32_e32 v32, v48
	s_nop 1
	v_permlane32_swap_b32_e32 v48, v32
	v_mfma_f32_32x32x16_f16 v[16:31], v[36:39], v[66:69], v[16:31]
	s_and_saveexec_b64 s[4:5], s[0:1]
	v_add_f32_e32 v32, v48, v32
	ds_write_b32 v218, v32 offset:49280
	s_or_b64 exec, exec, s[4:5]
	s_waitcnt lgkmcnt(0)
	ds_read_b128 v[32:35], v212 offset:49280
	ds_read_b128 v[36:39], v212 offset:49312
	s_lshl_b32 s4, s19, 12
	v_or_b32_e32 v48, s4, v201
	v_lshl_add_u32 v48, v191, 1, v48
	s_waitcnt lgkmcnt(1)
	v_rcp_f32_e32 v40, v32
	v_rcp_f32_e32 v41, v33
	v_rcp_f32_e32 v42, v34
	v_rcp_f32_e32 v43, v35
	v_fma_mixlo_f16 v0, v0, v40, 0
	ds_write_b16 v48, v0 offset:51200
	v_fma_mixlo_f16 v0, v16, v40, 0
	ds_write_b16 v48, v0 offset:51264
	v_fma_mixlo_f16 v0, v1, v41, 0
	ds_write_b16 v48, v0 offset:51328
	v_fma_mixlo_f16 v0, v17, v41, 0
	s_waitcnt lgkmcnt(3)
	v_rcp_f32_e32 v44, v36
	ds_write_b16 v48, v0 offset:51392
	v_fma_mixlo_f16 v0, v2, v42, 0
	ds_write_b16 v48, v0 offset:51456
	v_fma_mixlo_f16 v0, v18, v42, 0
	v_rcp_f32_e32 v45, v37
	ds_write_b16 v48, v0 offset:51520
	v_fma_mixlo_f16 v0, v3, v43, 0
	ds_read_b128 v[32:35], v212 offset:49344
	ds_write_b16 v48, v0 offset:51584
	v_fma_mixlo_f16 v0, v19, v43, 0
	v_rcp_f32_e32 v46, v38
	ds_write_b16 v48, v0 offset:51648
	v_fma_mixlo_f16 v0, v4, v44, 0
	ds_write_b16 v48, v0 offset:52224
	v_fma_mixlo_f16 v0, v20, v44, 0
	v_rcp_f32_e32 v47, v39
	ds_write_b16 v48, v0 offset:52288
	v_fma_mixlo_f16 v0, v5, v45, 0
	ds_write_b16 v48, v0 offset:52352
	v_fma_mixlo_f16 v0, v21, v45, 0
	ds_read_b128 v[36:39], v212 offset:49376
	s_waitcnt lgkmcnt(6)
	v_rcp_f32_e32 v32, v32
	ds_write_b16 v48, v0 offset:52416
	v_fma_mixlo_f16 v0, v6, v46, 0
	ds_write_b16 v48, v0 offset:52480
	v_fma_mixlo_f16 v0, v22, v46, 0
	v_rcp_f32_e32 v33, v33
	ds_write_b16 v48, v0 offset:52544
	v_fma_mixlo_f16 v0, v7, v47, 0
	ds_write_b16 v48, v0 offset:52608
	v_fma_mixlo_f16 v0, v23, v47, 0
	v_rcp_f32_e32 v34, v34
	ds_write_b16 v48, v0 offset:52672
	v_fma_mixlo_f16 v0, v8, v32, 0
	ds_write_b16 v48, v0 offset:53248
	v_fma_mixlo_f16 v0, v24, v32, 0
	v_rcp_f32_e32 v35, v35
	ds_write_b16 v48, v0 offset:53312
	v_fma_mixlo_f16 v0, v9, v33, 0
	ds_write_b16 v48, v0 offset:53376
	v_fma_mixlo_f16 v0, v25, v33, 0
	s_waitcnt lgkmcnt(8)
	v_rcp_f32_e32 v36, v36
	ds_write_b16 v48, v0 offset:53440
	v_fma_mixlo_f16 v0, v10, v34, 0
	ds_write_b16 v48, v0 offset:53504
	v_fma_mixlo_f16 v0, v26, v34, 0
	v_rcp_f32_e32 v37, v37
	ds_write_b16 v48, v0 offset:53568
	v_fma_mixlo_f16 v0, v11, v35, 0
	ds_write_b16 v48, v0 offset:53632
	v_fma_mixlo_f16 v0, v27, v35, 0
	v_rcp_f32_e32 v38, v38
	ds_write_b16 v48, v0 offset:53696
	v_fma_mixlo_f16 v0, v12, v36, 0
	ds_write_b16 v48, v0 offset:54272
	v_fma_mixlo_f16 v0, v28, v36, 0
	v_rcp_f32_e32 v39, v39
	ds_write_b16 v48, v0 offset:54336
	v_fma_mixlo_f16 v0, v13, v37, 0
	ds_write_b16 v48, v0 offset:54400
	v_fma_mixlo_f16 v0, v29, v37, 0
	ds_write_b16 v48, v0 offset:54464
	v_fma_mixlo_f16 v0, v14, v38, 0
	ds_write_b16 v48, v0 offset:54528
	v_fma_mixlo_f16 v0, v30, v38, 0
	ds_write_b16 v48, v0 offset:54592
	v_fma_mixlo_f16 v0, v15, v39, 0
	s_or_b64 s[0:1], s[2:3], s[6:7]
	ds_write_b16 v48, v0 offset:54656
	v_fma_mixlo_f16 v0, v31, v39, 0
	s_add_u32 s0, s18, s0
	ds_write_b16 v48, v0 offset:54720
	v_or_b32_e32 v12, s4, v213
	s_addc_u32 s1, 0, s1
	s_waitcnt lgkmcnt(0)
	v_lshl_add_u64 v[8:9], s[0:1], 0, v[194:195]
	v_add_u32_e32 v0, v12, v214
	ds_read_b128 v[0:3], v0 offset:51200
	v_or_b32_e32 v4, v8, v190
	v_mov_b32_e32 v5, v9
	v_lshlrev_b64 v[4:5], 6, v[4:5]
	v_lshl_add_u64 v[10:11], v[188:189], 0, v[4:5]
	v_add_u32_e32 v4, v12, v215
	ds_read_b128 v[4:7], v4 offset:51200
	s_waitcnt lgkmcnt(1)
	global_store_dwordx4 v[10:11], v[0:3], off sc1
	s_nop 1
	v_or_b32_e32 v0, v8, v196
	v_mov_b32_e32 v1, v9
	v_lshlrev_b64 v[0:1], 6, v[0:1]
	v_lshl_add_u64 v[0:1], v[188:189], 0, v[0:1]
	s_waitcnt lgkmcnt(0)
	global_store_dwordx4 v[0:1], v[4:7], off sc1
	v_add_u32_e32 v0, v12, v216
	ds_read_b128 v[0:3], v0 offset:51200
	v_or_b32_e32 v4, v8, v198
	v_mov_b32_e32 v5, v9
	v_lshlrev_b64 v[4:5], 6, v[4:5]
	v_lshl_add_u64 v[10:11], v[188:189], 0, v[4:5]
	v_add_u32_e32 v4, v12, v217
	ds_read_b128 v[4:7], v4 offset:51200
	v_or_b32_e32 v8, v8, v200
	s_waitcnt lgkmcnt(1)
	global_store_dwordx4 v[10:11], v[0:3], off sc1
	s_nop 1
	v_lshlrev_b64 v[0:1], 6, v[8:9]
	v_lshl_add_u64 v[0:1], v[188:189], 0, v[0:1]
	s_waitcnt lgkmcnt(0)
	global_store_dwordx4 v[0:1], v[4:7], off sc1
	s_waitcnt lgkmcnt(0)
	s_barrier
	s_endpgm

	.text
	.protected	_ZN2g34gemmILi4ELi1EEEvPKDF16_S2_PvPKfiiff
	.globl	_ZN2g34gemmILi4ELi1EEEvPKDF16_S2_PvPKfiiff
	.p2align	8
	.type	_ZN2g34gemmILi4ELi1EEEvPKDF16_S2_PvPKfiiff,@function

	.amdhsa_kernel _ZN2g34gemmILi4ELi1EEEvPKDF16_S2_PvPKfiiff
		.amdhsa_group_segment_fixed_size 98304
		.amdhsa_private_segment_fixed_size 0
		.amdhsa_kernarg_size 48
		.amdhsa_user_sgpr_count 2
		.amdhsa_user_sgpr_dispatch_ptr 0
		.amdhsa_user_sgpr_queue_ptr 0
		.amdhsa_user_sgpr_kernarg_segment_ptr 1
		.amdhsa_user_sgpr_dispatch_id 0
		.amdhsa_user_sgpr_kernarg_preload_length 0
		.amdhsa_user_sgpr_kernarg_preload_offset 0
		.amdhsa_user_sgpr_private_segment_size 0
		.amdhsa_uses_dynamic_stack 0
		.amdhsa_enable_private_segment 0
		.amdhsa_system_sgpr_workgroup_id_x 1
		.amdhsa_system_sgpr_workgroup_id_y 0
		.amdhsa_system_sgpr_workgroup_id_z 0
		.amdhsa_system_sgpr_workgroup_info 0
		.amdhsa_system_vgpr_workitem_id 0
		.amdhsa_next_free_vgpr 169
		.amdhsa_next_free_sgpr 96
		.amdhsa_accum_offset 144
		.amdhsa_reserve_vcc 0
		.amdhsa_float_round_mode_32 0
		.amdhsa_float_round_mode_16_64 0
		.amdhsa_float_denorm_mode_32 3
		.amdhsa_float_denorm_mode_16_64 3
		.amdhsa_dx10_clamp 1
		.amdhsa_ieee_mode 1
		.amdhsa_fp16_overflow 0
		.amdhsa_tg_split 0
		.amdhsa_exception_fp_ieee_invalid_op 0
		.amdhsa_exception_fp_denorm_src 0
		.amdhsa_exception_fp_ieee_div_zero 0
		.amdhsa_exception_fp_ieee_overflow 0
		.amdhsa_exception_fp_ieee_underflow 0
		.amdhsa_exception_fp_ieee_inexact 0
		.amdhsa_exception_int_div_zero 0
	.end_amdhsa_kernel
	.text
.Lfunc_end3:
	.size	_ZN2g34gemmILi4ELi1EEEvPKDF16_S2_PvPKfiiff, .Lfunc_end3-_ZN2g34gemmILi4ELi1EEEvPKDF16_S2_PvPKfiiff
	.set _ZN2g34gemmILi4ELi1EEEvPKDF16_S2_PvPKfiiff.num_vgpr, 141
	.set _ZN2g34gemmILi4ELi1EEEvPKDF16_S2_PvPKfiiff.num_agpr, 0
	.set _ZN2g34gemmILi4ELi1EEEvPKDF16_S2_PvPKfiiff.numbered_sgpr, 39
	.set _ZN2g34gemmILi4ELi1EEEvPKDF16_S2_PvPKfiiff.num_named_barrier, 0
	.set _ZN2g34gemmILi4ELi1EEEvPKDF16_S2_PvPKfiiff.private_seg_size, 0
	.set _ZN2g34gemmILi4ELi1EEEvPKDF16_S2_PvPKfiiff.uses_vcc, 0
	.set _ZN2g34gemmILi4ELi1EEEvPKDF16_S2_PvPKfiiff.uses_flat_scratch, 0
	.set _ZN2g34gemmILi4ELi1EEEvPKDF16_S2_PvPKfiiff.has_dyn_sized_stack, 0
	.set _ZN2g34gemmILi4ELi1EEEvPKDF16_S2_PvPKfiiff.has_recursion, 0
	.set _ZN2g34gemmILi4ELi1EEEvPKDF16_S2_PvPKfiiff.has_indirect_call, 0
